# pools repartition (prologue 832 items; layer-1 weights converted in dense-up idle round; attention pools 4112/4112) + early claim + adaLN 2x unroll + q2=1
# speedup vs baseline: 1.0119x; 1.0018x over previous
.LBB0_538:
	s_cmp_gt_u32 s16, 20
	s_cbranch_scc1 .Lec_0_skip
	s_and_saveexec_b64 s[2:3], s[0:1]
	s_cbranch_execz .Lec_0_rest
	v_readlane_b32 s30, v254, 52
	v_readlane_b32 s31, v254, 53
	v_mov_b32_e32 v253, 1
	s_nop 4
	global_atomic_add v253, v75, v253, s[30:31] offset:1280 sc0
.Lec_0_rest:
	s_or_b64 exec, exec, s[2:3]
.Lec_0_skip:
	s_mov_b32 s19, s20
	s_mov_b32 s10, s84
	s_mov_b32 s78, s21
	s_mov_b32 s69, s13
	s_mov_b32 s12, s18
	s_mov_b32 s68, s11
	s_mov_b64 s[80:81], s[82:83]
	s_mov_b64 s[30:31], -1
	s_mov_b64 s[2:3], 0
	s_cmp_lt_i32 s20, 2
	s_mov_b64 s[28:29], 0
	s_cbranch_scc1 .LBB0_545
	s_cmp_eq_u32 s19, 2
	s_mov_b64 s[28:29], -1
	s_cbranch_scc0 .LBB0_541
	s_waitcnt vmcnt(12)
	v_mul_f32_e32 v74, 0x44800000, v14
	v_mul_f32_e32 v69, 0x44800000, v10
	v_med3_f32 v86, v74, s66, v71
	s_waitcnt vmcnt(9)
	v_mul_f32_e32 v74, 0x44800000, v26
	v_med3_f32 v82, v69, s66, v71
	s_waitcnt vmcnt(8)
	v_mul_f32_e32 v77, 0x44800000, v30
	v_med3_f32 v83, v74, s66, v71
	v_mul_f32_e32 v67, 0x44800000, v6
	v_mul_f32_e32 v69, 0x44800000, v22
	v_med3_f32 v87, v77, s66, v71
	v_pk_add_f32 v[82:83], v[82:83], s[72:73] op_sel_hi:[1,0]
	v_mul_f32_e32 v66, 0x44800000, v2
	v_med3_f32 v68, v67, s66, v71
	v_mul_f32_e32 v67, 0x44800000, v18
	v_med3_f32 v69, v69, s66, v71
	v_pk_add_f32 v[86:87], v[86:87], s[72:73] op_sel_hi:[1,0]
	v_lshlrev_b32_e32 v74, 16, v83
	v_lshlrev_b32_e32 v77, 16, v82
	v_med3_f32 v66, v66, s66, v71
	v_med3_f32 v67, v67, s66, v71
	v_pk_add_f32 v[68:69], v[68:69], s[72:73] op_sel_hi:[1,0]
	v_and_b32_e32 v74, 0xff0000, v74
	v_and_b32_e32 v77, 0xff0000, v77
	v_lshlrev_b32_e32 v79, 24, v87
	v_lshlrev_b32_e32 v82, 24, v86
	v_pk_add_f32 v[66:67], v[66:67], s[72:73] op_sel_hi:[1,0]
	v_lshlrev_b32_e32 v69, 8, v69
	v_or_b32_e32 v74, v74, v79
	v_or_b32_e32 v77, v77, v82
	v_and_b32_e32 v69, 0xff00, v69
	v_or_b32_sdwa v67, v74, v67 dst_sel:DWORD dst_unused:UNUSED_PAD src0_sel:DWORD src1_sel:BYTE_0
	v_or_b32_sdwa v66, v77, v66 dst_sel:DWORD dst_unused:UNUSED_PAD src0_sel:DWORD src1_sel:BYTE_0
	s_waitcnt vmcnt(5)
	v_mul_f32_e32 v74, 0x44800000, v42
	s_waitcnt vmcnt(4)
	v_mul_f32_e32 v77, 0x44800000, v46
	v_or_b32_e32 v67, v67, v69
	v_mul_f32_e32 v69, 0x44800000, v38
	v_med3_f32 v86, v74, s66, v71
	v_med3_f32 v88, v77, s66, v71
	s_waitcnt vmcnt(2)
	v_mul_f32_e32 v74, 0x44800000, v54
	s_waitcnt vmcnt(1)
	v_mul_f32_e32 v77, 0x44800000, v58
	v_lshlrev_b32_e32 v68, 8, v68
	v_med3_f32 v82, v69, s66, v71
	s_waitcnt vmcnt(0)
	v_mul_f32_e32 v79, 0x44800000, v62
	v_med3_f32 v83, v74, s66, v71
	v_med3_f32 v87, v77, s66, v71
	v_and_b32_e32 v68, 0xff00, v68
	v_med3_f32 v89, v79, s66, v71
	v_pk_add_f32 v[82:83], v[82:83], s[72:73] op_sel_hi:[1,0]
	v_pk_add_f32 v[86:87], v[86:87], s[72:73] op_sel_hi:[1,0]
	v_or_b32_e32 v66, v66, v68
	v_mul_f32_e32 v68, 0x44800000, v34
	v_mul_f32_e32 v69, 0x44800000, v50
	v_pk_add_f32 v[88:89], v[88:89], s[72:73] op_sel_hi:[1,0]
	v_lshlrev_b32_e32 v77, 8, v82
	v_lshlrev_b32_e32 v79, 16, v87
	v_lshlrev_b32_e32 v82, 16, v86
	v_med3_f32 v68, v68, s66, v71
	v_med3_f32 v69, v69, s66, v71
	v_lshlrev_b32_e32 v74, 8, v83
	v_and_b32_e32 v79, 0xff0000, v79
	v_and_b32_e32 v82, 0xff0000, v82
	v_lshlrev_b32_e32 v83, 24, v89
	v_lshlrev_b32_e32 v85, 24, v88
	v_pk_add_f32 v[68:69], v[68:69], s[72:73] op_sel_hi:[1,0]
	v_or_b32_e32 v79, v79, v83
	v_or_b32_e32 v82, v82, v85
	v_and_b32_e32 v74, 0xff00, v74
	v_and_b32_e32 v77, 0xff00, v77
	v_or_b32_sdwa v69, v79, v69 dst_sel:DWORD dst_unused:UNUSED_PAD src0_sel:DWORD src1_sel:BYTE_0
	v_or_b32_sdwa v68, v82, v68 dst_sel:DWORD dst_unused:UNUSED_PAD src0_sel:DWORD src1_sel:BYTE_0
	v_or_b32_e32 v69, v69, v74
	v_or_b32_e32 v68, v68, v77
	v_add_u32_e32 v74, v199, v198
	v_mul_f32_e32 v77, 0x44800000, v15
	ds_write_b128 v74, v[66:69]
	v_mul_f32_e32 v69, 0x44800000, v11
	v_med3_f32 v86, v77, s66, v71
	v_mul_f32_e32 v77, 0x44800000, v27
	v_med3_f32 v82, v69, s66, v71
	v_mul_f32_e32 v79, 0x44800000, v31
	v_med3_f32 v83, v77, s66, v71
	v_mul_f32_e32 v67, 0x44800000, v7
	v_mul_f32_e32 v69, 0x44800000, v23
	v_med3_f32 v87, v79, s66, v71
	v_pk_add_f32 v[82:83], v[82:83], s[72:73] op_sel_hi:[1,0]
	v_mul_f32_e32 v66, 0x44800000, v3
	v_med3_f32 v68, v67, s66, v71
	v_mul_f32_e32 v67, 0x44800000, v19
	v_med3_f32 v69, v69, s66, v71
	v_pk_add_f32 v[86:87], v[86:87], s[72:73] op_sel_hi:[1,0]
	v_lshlrev_b32_e32 v77, 16, v83
	v_lshlrev_b32_e32 v79, 16, v82
	v_med3_f32 v66, v66, s66, v71
	v_med3_f32 v67, v67, s66, v71
	v_pk_add_f32 v[68:69], v[68:69], s[72:73] op_sel_hi:[1,0]
	v_and_b32_e32 v77, 0xff0000, v77
	v_and_b32_e32 v79, 0xff0000, v79
	v_lshlrev_b32_e32 v82, 24, v87
	v_lshlrev_b32_e32 v83, 24, v86
	v_pk_add_f32 v[66:67], v[66:67], s[72:73] op_sel_hi:[1,0]
	v_lshlrev_b32_e32 v69, 8, v69
	v_or_b32_e32 v77, v77, v82
	v_or_b32_e32 v79, v79, v83
	v_and_b32_e32 v69, 0xff00, v69
	v_or_b32_sdwa v67, v77, v67 dst_sel:DWORD dst_unused:UNUSED_PAD src0_sel:DWORD src1_sel:BYTE_0
	v_or_b32_sdwa v66, v79, v66 dst_sel:DWORD dst_unused:UNUSED_PAD src0_sel:DWORD src1_sel:BYTE_0
	v_mul_f32_e32 v77, 0x44800000, v43
	v_mul_f32_e32 v79, 0x44800000, v47
	v_or_b32_e32 v67, v67, v69
	v_mul_f32_e32 v69, 0x44800000, v39
	v_med3_f32 v86, v77, s66, v71
	v_med3_f32 v88, v79, s66, v71
	v_mul_f32_e32 v77, 0x44800000, v55
	v_mul_f32_e32 v79, 0x44800000, v59
	v_lshlrev_b32_e32 v68, 8, v68
	v_med3_f32 v82, v69, s66, v71
	v_mul_f32_e32 v85, 0x44800000, v63
	v_med3_f32 v83, v77, s66, v71
	v_med3_f32 v87, v79, s66, v71
	v_and_b32_e32 v68, 0xff00, v68
	v_med3_f32 v89, v85, s66, v71
	v_pk_add_f32 v[82:83], v[82:83], s[72:73] op_sel_hi:[1,0]
	v_pk_add_f32 v[86:87], v[86:87], s[72:73] op_sel_hi:[1,0]
	v_or_b32_e32 v66, v66, v68
	v_mul_f32_e32 v68, 0x44800000, v35
	v_mul_f32_e32 v69, 0x44800000, v51
	v_pk_add_f32 v[88:89], v[88:89], s[72:73] op_sel_hi:[1,0]
	v_lshlrev_b32_e32 v77, 8, v83
	v_lshlrev_b32_e32 v79, 8, v82
	v_lshlrev_b32_e32 v82, 16, v87
	v_lshlrev_b32_e32 v83, 16, v86
	v_med3_f32 v68, v68, s66, v71
	v_med3_f32 v69, v69, s66, v71
	v_and_b32_e32 v82, 0xff0000, v82
	v_and_b32_e32 v83, 0xff0000, v83
	v_lshlrev_b32_e32 v85, 24, v89
	v_lshlrev_b32_e32 v86, 24, v88
	v_pk_add_f32 v[68:69], v[68:69], s[72:73] op_sel_hi:[1,0]
	v_or_b32_e32 v82, v82, v85
	v_or_b32_e32 v83, v83, v86
	v_and_b32_e32 v77, 0xff00, v77
	v_and_b32_e32 v79, 0xff00, v79
	v_or_b32_sdwa v69, v82, v69 dst_sel:DWORD dst_unused:UNUSED_PAD src0_sel:DWORD src1_sel:BYTE_0
	v_or_b32_sdwa v68, v83, v68 dst_sel:DWORD dst_unused:UNUSED_PAD src0_sel:DWORD src1_sel:BYTE_0
	v_or_b32_e32 v69, v69, v77
	v_or_b32_e32 v68, v68, v79
	v_mul_f32_e32 v77, 0x44800000, v16
	ds_write_b128 v74, v[66:69] offset:528
	v_mul_f32_e32 v69, 0x44800000, v12
	v_med3_f32 v86, v77, s66, v71
	v_mul_f32_e32 v77, 0x44800000, v28
	v_med3_f32 v82, v69, s66, v71
	v_mul_f32_e32 v79, 0x44800000, v32
	v_med3_f32 v83, v77, s66, v71
	v_mul_f32_e32 v67, 0x44800000, v8
	v_mul_f32_e32 v69, 0x44800000, v24
	v_med3_f32 v87, v79, s66, v71
	v_pk_add_f32 v[82:83], v[82:83], s[72:73] op_sel_hi:[1,0]
	v_mul_f32_e32 v66, 0x44800000, v4
	v_med3_f32 v68, v67, s66, v71
	v_mul_f32_e32 v67, 0x44800000, v20
	v_med3_f32 v69, v69, s66, v71
	v_pk_add_f32 v[86:87], v[86:87], s[72:73] op_sel_hi:[1,0]
	v_lshlrev_b32_e32 v77, 16, v83
	v_lshlrev_b32_e32 v79, 16, v82
	v_med3_f32 v66, v66, s66, v71
	v_med3_f32 v67, v67, s66, v71
	v_pk_add_f32 v[68:69], v[68:69], s[72:73] op_sel_hi:[1,0]
	v_and_b32_e32 v77, 0xff0000, v77
	v_and_b32_e32 v79, 0xff0000, v79
	v_lshlrev_b32_e32 v82, 24, v87
	v_lshlrev_b32_e32 v83, 24, v86
	v_pk_add_f32 v[66:67], v[66:67], s[72:73] op_sel_hi:[1,0]
	v_lshlrev_b32_e32 v69, 8, v69
	v_or_b32_e32 v77, v77, v82
	v_or_b32_e32 v79, v79, v83
	v_and_b32_e32 v69, 0xff00, v69
	v_or_b32_sdwa v67, v77, v67 dst_sel:DWORD dst_unused:UNUSED_PAD src0_sel:DWORD src1_sel:BYTE_0
	v_or_b32_sdwa v66, v79, v66 dst_sel:DWORD dst_unused:UNUSED_PAD src0_sel:DWORD src1_sel:BYTE_0
	v_mul_f32_e32 v77, 0x44800000, v44
	v_mul_f32_e32 v79, 0x44800000, v48
	v_or_b32_e32 v67, v67, v69
	v_mul_f32_e32 v69, 0x44800000, v40
	v_med3_f32 v86, v77, s66, v71
	v_med3_f32 v88, v79, s66, v71
	v_mul_f32_e32 v77, 0x44800000, v56
	v_mul_f32_e32 v79, 0x44800000, v60
	v_lshlrev_b32_e32 v68, 8, v68
	v_med3_f32 v82, v69, s66, v71
	v_mul_f32_e32 v85, 0x44800000, v64
	v_med3_f32 v83, v77, s66, v71
	v_med3_f32 v87, v79, s66, v71
	v_and_b32_e32 v68, 0xff00, v68
	v_med3_f32 v89, v85, s66, v71
	v_pk_add_f32 v[82:83], v[82:83], s[72:73] op_sel_hi:[1,0]
	v_pk_add_f32 v[86:87], v[86:87], s[72:73] op_sel_hi:[1,0]
	v_or_b32_e32 v66, v66, v68
	v_mul_f32_e32 v68, 0x44800000, v36
	v_mul_f32_e32 v69, 0x44800000, v52
	v_pk_add_f32 v[88:89], v[88:89], s[72:73] op_sel_hi:[1,0]
	v_lshlrev_b32_e32 v77, 8, v83
	v_lshlrev_b32_e32 v79, 8, v82
	v_lshlrev_b32_e32 v82, 16, v87
	v_lshlrev_b32_e32 v83, 16, v86
	v_med3_f32 v68, v68, s66, v71
	v_med3_f32 v69, v69, s66, v71
	v_and_b32_e32 v82, 0xff0000, v82
	v_and_b32_e32 v83, 0xff0000, v83
	v_lshlrev_b32_e32 v85, 24, v89
	v_lshlrev_b32_e32 v86, 24, v88
	v_pk_add_f32 v[68:69], v[68:69], s[72:73] op_sel_hi:[1,0]
	v_or_b32_e32 v82, v82, v85
	v_or_b32_e32 v83, v83, v86
	v_and_b32_e32 v77, 0xff00, v77
	v_and_b32_e32 v79, 0xff00, v79
	v_or_b32_sdwa v69, v82, v69 dst_sel:DWORD dst_unused:UNUSED_PAD src0_sel:DWORD src1_sel:BYTE_0
	v_or_b32_sdwa v68, v83, v68 dst_sel:DWORD dst_unused:UNUSED_PAD src0_sel:DWORD src1_sel:BYTE_0
	v_or_b32_e32 v69, v69, v77
	v_or_b32_e32 v68, v68, v79
	v_mul_f32_e32 v77, 0x44800000, v17
	ds_write_b128 v74, v[66:69] offset:1056
	v_mul_f32_e32 v69, 0x44800000, v13
	v_med3_f32 v86, v77, s66, v71
	v_mul_f32_e32 v77, 0x44800000, v29
	v_med3_f32 v82, v69, s66, v71
	v_mul_f32_e32 v79, 0x44800000, v33
	v_med3_f32 v83, v77, s66, v71
	v_mul_f32_e32 v67, 0x44800000, v9
	v_mul_f32_e32 v69, 0x44800000, v25
	v_med3_f32 v87, v79, s66, v71
	v_pk_add_f32 v[82:83], v[82:83], s[72:73] op_sel_hi:[1,0]
	v_mul_f32_e32 v66, 0x44800000, v5
	v_med3_f32 v68, v67, s66, v71
	v_mul_f32_e32 v67, 0x44800000, v21
	v_med3_f32 v69, v69, s66, v71
	v_pk_add_f32 v[86:87], v[86:87], s[72:73] op_sel_hi:[1,0]
	v_lshlrev_b32_e32 v77, 16, v83
	v_lshlrev_b32_e32 v79, 16, v82
	v_med3_f32 v66, v66, s66, v71
	v_med3_f32 v67, v67, s66, v71
	v_pk_add_f32 v[68:69], v[68:69], s[72:73] op_sel_hi:[1,0]
	v_and_b32_e32 v77, 0xff0000, v77
	v_and_b32_e32 v79, 0xff0000, v79
	v_lshlrev_b32_e32 v82, 24, v87
	v_lshlrev_b32_e32 v83, 24, v86
	v_pk_add_f32 v[66:67], v[66:67], s[72:73] op_sel_hi:[1,0]
	v_lshlrev_b32_e32 v69, 8, v69
	v_or_b32_e32 v77, v77, v82
	v_or_b32_e32 v79, v79, v83
	v_and_b32_e32 v69, 0xff00, v69
	v_or_b32_sdwa v67, v77, v67 dst_sel:DWORD dst_unused:UNUSED_PAD src0_sel:DWORD src1_sel:BYTE_0
	v_or_b32_sdwa v66, v79, v66 dst_sel:DWORD dst_unused:UNUSED_PAD src0_sel:DWORD src1_sel:BYTE_0
	v_mul_f32_e32 v77, 0x44800000, v45
	v_mul_f32_e32 v79, 0x44800000, v49
	v_or_b32_e32 v67, v67, v69
	v_mul_f32_e32 v69, 0x44800000, v41
	v_med3_f32 v86, v77, s66, v71
	v_med3_f32 v88, v79, s66, v71
	v_mul_f32_e32 v77, 0x44800000, v57
	v_mul_f32_e32 v79, 0x44800000, v61
	v_lshlrev_b32_e32 v68, 8, v68
	v_med3_f32 v82, v69, s66, v71
	v_mul_f32_e32 v85, 0x44800000, v65
	v_med3_f32 v83, v77, s66, v71
	v_med3_f32 v87, v79, s66, v71
	v_and_b32_e32 v68, 0xff00, v68
	v_med3_f32 v89, v85, s66, v71
	v_pk_add_f32 v[82:83], v[82:83], s[72:73] op_sel_hi:[1,0]
	v_pk_add_f32 v[86:87], v[86:87], s[72:73] op_sel_hi:[1,0]
	v_or_b32_e32 v66, v66, v68
	v_mul_f32_e32 v68, 0x44800000, v37
	v_mul_f32_e32 v69, 0x44800000, v53
	v_pk_add_f32 v[88:89], v[88:89], s[72:73] op_sel_hi:[1,0]
	v_lshlrev_b32_e32 v77, 8, v83
	v_lshlrev_b32_e32 v79, 8, v82
	v_lshlrev_b32_e32 v82, 16, v87
	v_lshlrev_b32_e32 v83, 16, v86
	v_med3_f32 v68, v68, s66, v71
	v_med3_f32 v69, v69, s66, v71
	v_and_b32_e32 v82, 0xff0000, v82
	v_and_b32_e32 v83, 0xff0000, v83
	v_lshlrev_b32_e32 v85, 24, v89
	v_lshlrev_b32_e32 v86, 24, v88
	v_pk_add_f32 v[68:69], v[68:69], s[72:73] op_sel_hi:[1,0]
	v_or_b32_e32 v82, v82, v85
	v_or_b32_e32 v83, v83, v86
	v_and_b32_e32 v77, 0xff00, v77
	v_and_b32_e32 v79, 0xff00, v79
	v_or_b32_sdwa v69, v82, v69 dst_sel:DWORD dst_unused:UNUSED_PAD src0_sel:DWORD src1_sel:BYTE_0
	v_or_b32_sdwa v68, v83, v68 dst_sel:DWORD dst_unused:UNUSED_PAD src0_sel:DWORD src1_sel:BYTE_0
	v_or_b32_e32 v69, v69, v77
	v_or_b32_e32 v68, v68, v79
	ds_write_b128 v74, v[66:69] offset:1584
	s_mov_b64 s[28:29], 0

.LBB0_549:
	s_cmp_gt_u32 s16, 20
	v_mov_b32_e32 v66, 0x1690
	s_cbranch_scc1 .LBB0_553
	s_mov_b64 s[30:31], exec
	v_mbcnt_lo_u32_b32 v66, s30, 0
	v_mbcnt_hi_u32_b32 v66, s31, v66
	v_cmp_eq_u32_e32 vcc, 0, v66
	s_and_saveexec_b64 s[28:29], vcc
	s_cbranch_execz .LBB0_552
	s_bcnt1_i32_b64 s11, s[30:31]
	v_readlane_b32 s36, v254, 38
	v_mov_b32_e32 v67, s11
	v_readlane_b32 s50, v254, 52
	v_readlane_b32 s51, v254, 53
	v_readlane_b32 s37, v254, 39
	v_readlane_b32 s38, v254, 40
	v_readlane_b32 s39, v254, 41
	v_readlane_b32 s40, v254, 42
	v_readlane_b32 s41, v254, 43
	v_mov_b32_e32 v67, v253
	v_readlane_b32 s42, v254, 44
	v_readlane_b32 s43, v254, 45
	v_readlane_b32 s44, v254, 46
	v_readlane_b32 s45, v254, 47
	v_readlane_b32 s46, v254, 48
	v_readlane_b32 s47, v254, 49
	v_readlane_b32 s48, v254, 50
	v_readlane_b32 s49, v254, 51

.LBB0_724:
	s_cmpk_lt_i32 s8, 0x80
	s_cselect_b32 s6, 1, 0
	s_and_b64 s[2:3], s[4:5], exec
	s_cselect_b32 s16, s6, 4
	s_cmp_lg_u32 s16, 0
	v_mov_b32_e32 v206, v205
	v_mov_b32_e32 v207, v213
	v_mov_b32_e32 v213, v209
	v_mov_b32_e32 v209, v211
	v_or_b32_e32 v211, 0x60, v1
	s_waitcnt lgkmcnt(0)
	s_barrier
	s_cbranch_scc0 .LBB0_931
	s_and_saveexec_b64 s[2:3], s[0:1]
	v_readlane_b32 s36, v254, 38
	v_readlane_b32 s46, v254, 48
	v_readlane_b32 s47, v254, 49
	v_readlane_b32 s50, v254, 52
	v_readlane_b32 s51, v254, 53
	v_readlane_b32 s37, v254, 39
	v_readlane_b32 s38, v254, 40
	v_readlane_b32 s39, v254, 41
	v_readlane_b32 s40, v254, 42
	v_readlane_b32 s41, v254, 43
	v_readlane_b32 s42, v254, 44
	v_readlane_b32 s43, v254, 45
	v_readlane_b32 s44, v254, 46
	v_readlane_b32 s45, v254, 47
	v_readlane_b32 s48, v254, 50
	v_readlane_b32 s49, v254, 51
	s_cbranch_execz .LBB0_729
	s_mov_b64 s[6:7], exec
	s_waitcnt vmcnt(15)
	v_mbcnt_lo_u32_b32 v2, s6, 0
	v_mbcnt_hi_u32_b32 v2, s7, v2
	v_cmp_eq_u32_e32 vcc, 0, v2
	s_and_saveexec_b64 s[4:5], vcc
	s_cbranch_execz .LBB0_728
	s_bcnt1_i32_b64 s6, s[6:7]
	v_mov_b32_e32 v3, 0
	v_mov_b32_e32 v4, s6
	global_atomic_add v3, v3, v4, s[50:51] offset:1280 sc0

.LBB0_779:
	s_cmp_ge_u32 s17, s16
	s_cbranch_scc1 .Lec_1_skip
	s_and_saveexec_b64 s[2:3], s[0:1]
	s_cbranch_execz .Lec_1_rest
	v_readlane_b32 s30, v254, 52
	v_readlane_b32 s31, v254, 53
	v_mov_b32_e32 v253, 1
	s_nop 4
	global_atomic_add v253, v71, v253, s[30:31] offset:1280 sc0
.Lec_1_rest:
	s_or_b64 exec, exec, s[2:3]
.Lec_1_skip:
	v_readlane_b32 s36, v254, 38
	s_mov_b32 s19, s20
	s_mov_b32 s10, s82
	s_mov_b32 s74, s21
	s_mov_b32 s67, s13
	s_mov_b32 s12, s18
	s_mov_b32 s66, s11
	s_mov_b64 s[78:79], s[80:81]
	s_mov_b64 s[30:31], -1
	s_mov_b64 s[2:3], 0
	s_cmp_lt_i32 s20, 2
	s_mov_b64 s[28:29], 0
	v_readlane_b32 s50, v254, 52
	v_readlane_b32 s51, v254, 53
	v_readlane_b32 s37, v254, 39
	v_readlane_b32 s38, v254, 40
	v_readlane_b32 s39, v254, 41
	v_readlane_b32 s40, v254, 42
	v_readlane_b32 s41, v254, 43
	v_readlane_b32 s42, v254, 44
	v_readlane_b32 s43, v254, 45
	v_readlane_b32 s44, v254, 46
	v_readlane_b32 s45, v254, 47
	v_readlane_b32 s46, v254, 48
	v_readlane_b32 s47, v254, 49
	v_readlane_b32 s48, v254, 50
	v_readlane_b32 s49, v254, 51
	s_cbranch_scc1 .LBB0_786
	s_cmp_eq_u32 s19, 2
	s_mov_b64 s[28:29], -1
	s_cbranch_scc0 .LBB0_782
	s_waitcnt vmcnt(12)
	v_mul_f32_e32 v70, 0x44800000, v14
	v_mul_f32_e32 v69, 0x44800000, v10
	v_med3_f32 v76, v70, s64, v72
	s_waitcnt vmcnt(9)
	v_mul_f32_e32 v70, 0x44800000, v26
	v_med3_f32 v74, v69, s64, v72
	s_waitcnt vmcnt(8)
	v_mul_f32_e32 v73, 0x44800000, v30
	v_med3_f32 v75, v70, s64, v72
	v_mul_f32_e32 v67, 0x44800000, v6
	v_mul_f32_e32 v69, 0x44800000, v22
	v_med3_f32 v77, v73, s64, v72
	v_pk_add_f32 v[74:75], v[74:75], s[56:57] op_sel_hi:[1,0]
	v_mul_f32_e32 v66, 0x44800000, v2
	v_med3_f32 v68, v67, s64, v72
	v_mul_f32_e32 v67, 0x44800000, v18
	v_med3_f32 v69, v69, s64, v72
	v_pk_add_f32 v[76:77], v[76:77], s[56:57] op_sel_hi:[1,0]
	v_lshlrev_b32_e32 v70, 16, v75
	v_lshlrev_b32_e32 v73, 16, v74
	v_med3_f32 v66, v66, s64, v72
	v_med3_f32 v67, v67, s64, v72
	v_pk_add_f32 v[68:69], v[68:69], s[56:57] op_sel_hi:[1,0]
	v_and_b32_e32 v70, 0xff0000, v70
	v_and_b32_e32 v73, 0xff0000, v73
	v_lshlrev_b32_e32 v74, 24, v77
	v_lshlrev_b32_e32 v75, 24, v76
	v_pk_add_f32 v[66:67], v[66:67], s[56:57] op_sel_hi:[1,0]
	v_lshlrev_b32_e32 v69, 8, v69
	v_or_b32_e32 v70, v70, v74
	v_or_b32_e32 v73, v73, v75
	v_and_b32_e32 v69, 0xff00, v69
	v_or_b32_sdwa v67, v70, v67 dst_sel:DWORD dst_unused:UNUSED_PAD src0_sel:DWORD src1_sel:BYTE_0
	v_or_b32_sdwa v66, v73, v66 dst_sel:DWORD dst_unused:UNUSED_PAD src0_sel:DWORD src1_sel:BYTE_0
	s_waitcnt vmcnt(5)
	v_mul_f32_e32 v70, 0x44800000, v42
	s_waitcnt vmcnt(4)
	v_mul_f32_e32 v73, 0x44800000, v46
	v_or_b32_e32 v67, v67, v69
	v_mul_f32_e32 v69, 0x44800000, v38
	v_med3_f32 v76, v70, s64, v72
	v_med3_f32 v78, v73, s64, v72
	s_waitcnt vmcnt(2)
	v_mul_f32_e32 v70, 0x44800000, v54
	s_waitcnt vmcnt(1)
	v_mul_f32_e32 v73, 0x44800000, v58
	v_lshlrev_b32_e32 v68, 8, v68
	v_med3_f32 v74, v69, s64, v72
	s_waitcnt vmcnt(0)
	v_mul_f32_e32 v79, 0x44800000, v62
	v_med3_f32 v75, v70, s64, v72
	v_med3_f32 v77, v73, s64, v72
	v_and_b32_e32 v68, 0xff00, v68
	v_med3_f32 v79, v79, s64, v72
	v_pk_add_f32 v[74:75], v[74:75], s[56:57] op_sel_hi:[1,0]
	v_pk_add_f32 v[76:77], v[76:77], s[56:57] op_sel_hi:[1,0]
	v_or_b32_e32 v66, v66, v68
	v_mul_f32_e32 v68, 0x44800000, v34
	v_mul_f32_e32 v69, 0x44800000, v50
	v_pk_add_f32 v[78:79], v[78:79], s[56:57] op_sel_hi:[1,0]
	v_lshlrev_b32_e32 v70, 8, v75
	v_lshlrev_b32_e32 v73, 8, v74
	v_lshlrev_b32_e32 v74, 16, v77
	v_lshlrev_b32_e32 v75, 16, v76
	v_med3_f32 v68, v68, s64, v72
	v_med3_f32 v69, v69, s64, v72
	v_and_b32_e32 v74, 0xff0000, v74
	v_and_b32_e32 v75, 0xff0000, v75
	v_lshlrev_b32_e32 v76, 24, v79
	v_lshlrev_b32_e32 v77, 24, v78
	v_pk_add_f32 v[68:69], v[68:69], s[56:57] op_sel_hi:[1,0]
	v_or_b32_e32 v74, v74, v76
	v_or_b32_e32 v75, v75, v77
	v_and_b32_e32 v70, 0xff00, v70
	v_and_b32_e32 v73, 0xff00, v73
	v_or_b32_sdwa v69, v74, v69 dst_sel:DWORD dst_unused:UNUSED_PAD src0_sel:DWORD src1_sel:BYTE_0
	v_or_b32_sdwa v68, v75, v68 dst_sel:DWORD dst_unused:UNUSED_PAD src0_sel:DWORD src1_sel:BYTE_0
	v_or_b32_e32 v69, v69, v70
	v_or_b32_e32 v68, v68, v73
	v_add_u32_e32 v70, v199, v198
	v_mul_f32_e32 v73, 0x44800000, v15
	ds_write_b128 v70, v[66:69]
	v_mul_f32_e32 v69, 0x44800000, v11
	v_med3_f32 v76, v73, s64, v72
	v_mul_f32_e32 v73, 0x44800000, v27
	v_med3_f32 v74, v69, s64, v72
	v_mul_f32_e32 v77, 0x44800000, v31
	v_med3_f32 v75, v73, s64, v72
	v_mul_f32_e32 v67, 0x44800000, v7
	v_mul_f32_e32 v69, 0x44800000, v23
	v_med3_f32 v77, v77, s64, v72
	v_pk_add_f32 v[74:75], v[74:75], s[56:57] op_sel_hi:[1,0]
	v_mul_f32_e32 v66, 0x44800000, v3
	v_med3_f32 v68, v67, s64, v72
	v_mul_f32_e32 v67, 0x44800000, v19
	v_med3_f32 v69, v69, s64, v72
	v_pk_add_f32 v[76:77], v[76:77], s[56:57] op_sel_hi:[1,0]
	v_lshlrev_b32_e32 v73, 16, v75
	v_med3_f32 v66, v66, s64, v72
	v_med3_f32 v67, v67, s64, v72
	v_pk_add_f32 v[68:69], v[68:69], s[56:57] op_sel_hi:[1,0]
	v_and_b32_e32 v73, 0xff0000, v73
	v_lshlrev_b32_e32 v75, 24, v77
	v_pk_add_f32 v[66:67], v[66:67], s[56:57] op_sel_hi:[1,0]
	v_lshlrev_b32_e32 v69, 8, v69
	v_lshlrev_b32_e32 v74, 16, v74
	v_or_b32_e32 v73, v73, v75
	v_and_b32_e32 v69, 0xff00, v69
	v_and_b32_e32 v74, 0xff0000, v74
	v_lshlrev_b32_e32 v76, 24, v76
	v_or_b32_sdwa v67, v73, v67 dst_sel:DWORD dst_unused:UNUSED_PAD src0_sel:DWORD src1_sel:BYTE_0
	v_mul_f32_e32 v73, 0x44800000, v43
	v_or_b32_e32 v74, v74, v76
	v_or_b32_e32 v67, v67, v69
	v_mul_f32_e32 v69, 0x44800000, v39
	v_mul_f32_e32 v75, 0x44800000, v47
	v_med3_f32 v76, v73, s64, v72
	v_mul_f32_e32 v73, 0x44800000, v55
	v_mul_f32_e32 v77, 0x44800000, v59
	v_lshlrev_b32_e32 v68, 8, v68
	v_or_b32_sdwa v66, v74, v66 dst_sel:DWORD dst_unused:UNUSED_PAD src0_sel:DWORD src1_sel:BYTE_0
	v_med3_f32 v74, v69, s64, v72
	v_med3_f32 v78, v75, s64, v72
	v_mul_f32_e32 v79, 0x44800000, v63
	v_med3_f32 v75, v73, s64, v72
	v_med3_f32 v77, v77, s64, v72
	v_and_b32_e32 v68, 0xff00, v68
	v_med3_f32 v79, v79, s64, v72
	v_pk_add_f32 v[74:75], v[74:75], s[56:57] op_sel_hi:[1,0]
	v_pk_add_f32 v[76:77], v[76:77], s[56:57] op_sel_hi:[1,0]
	v_or_b32_e32 v66, v66, v68
	v_mul_f32_e32 v68, 0x44800000, v35
	v_mul_f32_e32 v69, 0x44800000, v51
	v_pk_add_f32 v[78:79], v[78:79], s[56:57] op_sel_hi:[1,0]
	v_lshlrev_b32_e32 v73, 8, v75
	v_lshlrev_b32_e32 v75, 16, v77
	v_lshlrev_b32_e32 v76, 16, v76
	v_med3_f32 v68, v68, s64, v72
	v_med3_f32 v69, v69, s64, v72
	v_and_b32_e32 v75, 0xff0000, v75
	v_and_b32_e32 v76, 0xff0000, v76
	v_lshlrev_b32_e32 v77, 24, v79
	v_lshlrev_b32_e32 v78, 24, v78
	v_pk_add_f32 v[68:69], v[68:69], s[56:57] op_sel_hi:[1,0]
	v_lshlrev_b32_e32 v74, 8, v74
	v_or_b32_e32 v75, v75, v77
	v_or_b32_e32 v76, v76, v78
	v_and_b32_e32 v73, 0xff00, v73
	v_and_b32_e32 v74, 0xff00, v74
	v_or_b32_sdwa v69, v75, v69 dst_sel:DWORD dst_unused:UNUSED_PAD src0_sel:DWORD src1_sel:BYTE_0
	v_or_b32_sdwa v68, v76, v68 dst_sel:DWORD dst_unused:UNUSED_PAD src0_sel:DWORD src1_sel:BYTE_0
	v_or_b32_e32 v69, v69, v73
	v_or_b32_e32 v68, v68, v74
	v_mul_f32_e32 v73, 0x44800000, v16
	ds_write_b128 v70, v[66:69] offset:528
	v_mul_f32_e32 v69, 0x44800000, v12
	v_med3_f32 v76, v73, s64, v72
	v_mul_f32_e32 v73, 0x44800000, v28
	v_med3_f32 v74, v69, s64, v72
	v_mul_f32_e32 v77, 0x44800000, v32
	v_med3_f32 v75, v73, s64, v72
	v_mul_f32_e32 v67, 0x44800000, v8
	v_mul_f32_e32 v69, 0x44800000, v24
	v_med3_f32 v77, v77, s64, v72
	v_pk_add_f32 v[74:75], v[74:75], s[56:57] op_sel_hi:[1,0]
	v_mul_f32_e32 v66, 0x44800000, v4
	v_med3_f32 v68, v67, s64, v72
	v_mul_f32_e32 v67, 0x44800000, v20
	v_med3_f32 v69, v69, s64, v72
	v_pk_add_f32 v[76:77], v[76:77], s[56:57] op_sel_hi:[1,0]
	v_lshlrev_b32_e32 v73, 16, v75
	v_med3_f32 v66, v66, s64, v72
	v_med3_f32 v67, v67, s64, v72
	v_pk_add_f32 v[68:69], v[68:69], s[56:57] op_sel_hi:[1,0]
	v_and_b32_e32 v73, 0xff0000, v73
	v_lshlrev_b32_e32 v75, 24, v77
	v_pk_add_f32 v[66:67], v[66:67], s[56:57] op_sel_hi:[1,0]
	v_lshlrev_b32_e32 v69, 8, v69
	v_lshlrev_b32_e32 v74, 16, v74
	v_or_b32_e32 v73, v73, v75
	v_and_b32_e32 v69, 0xff00, v69
	v_and_b32_e32 v74, 0xff0000, v74
	v_lshlrev_b32_e32 v76, 24, v76
	v_or_b32_sdwa v67, v73, v67 dst_sel:DWORD dst_unused:UNUSED_PAD src0_sel:DWORD src1_sel:BYTE_0
	v_mul_f32_e32 v73, 0x44800000, v44
	v_or_b32_e32 v74, v74, v76
	v_or_b32_e32 v67, v67, v69
	v_mul_f32_e32 v69, 0x44800000, v40
	v_mul_f32_e32 v75, 0x44800000, v48
	v_med3_f32 v76, v73, s64, v72
	v_mul_f32_e32 v73, 0x44800000, v56
	v_mul_f32_e32 v77, 0x44800000, v60
	v_lshlrev_b32_e32 v68, 8, v68
	v_or_b32_sdwa v66, v74, v66 dst_sel:DWORD dst_unused:UNUSED_PAD src0_sel:DWORD src1_sel:BYTE_0
	v_med3_f32 v74, v69, s64, v72
	v_med3_f32 v78, v75, s64, v72
	v_mul_f32_e32 v79, 0x44800000, v64
	v_med3_f32 v75, v73, s64, v72
	v_med3_f32 v77, v77, s64, v72
	v_and_b32_e32 v68, 0xff00, v68
	v_med3_f32 v79, v79, s64, v72
	v_pk_add_f32 v[74:75], v[74:75], s[56:57] op_sel_hi:[1,0]
	v_pk_add_f32 v[76:77], v[76:77], s[56:57] op_sel_hi:[1,0]
	v_or_b32_e32 v66, v66, v68
	v_mul_f32_e32 v68, 0x44800000, v36
	v_mul_f32_e32 v69, 0x44800000, v52
	v_pk_add_f32 v[78:79], v[78:79], s[56:57] op_sel_hi:[1,0]
	v_lshlrev_b32_e32 v73, 8, v75
	v_lshlrev_b32_e32 v75, 16, v77
	v_lshlrev_b32_e32 v76, 16, v76
	v_med3_f32 v68, v68, s64, v72
	v_med3_f32 v69, v69, s64, v72
	v_and_b32_e32 v75, 0xff0000, v75
	v_and_b32_e32 v76, 0xff0000, v76
	v_lshlrev_b32_e32 v77, 24, v79
	v_lshlrev_b32_e32 v78, 24, v78
	v_pk_add_f32 v[68:69], v[68:69], s[56:57] op_sel_hi:[1,0]
	v_lshlrev_b32_e32 v74, 8, v74
	v_or_b32_e32 v75, v75, v77
	v_or_b32_e32 v76, v76, v78
	v_and_b32_e32 v73, 0xff00, v73
	v_and_b32_e32 v74, 0xff00, v74
	v_or_b32_sdwa v69, v75, v69 dst_sel:DWORD dst_unused:UNUSED_PAD src0_sel:DWORD src1_sel:BYTE_0
	v_or_b32_sdwa v68, v76, v68 dst_sel:DWORD dst_unused:UNUSED_PAD src0_sel:DWORD src1_sel:BYTE_0
	v_or_b32_e32 v69, v69, v73
	v_or_b32_e32 v68, v68, v74
	v_mul_f32_e32 v73, 0x44800000, v17
	ds_write_b128 v70, v[66:69] offset:1056
	v_mul_f32_e32 v69, 0x44800000, v13
	v_med3_f32 v76, v73, s64, v72
	v_mul_f32_e32 v73, 0x44800000, v29
	v_med3_f32 v74, v69, s64, v72
	v_mul_f32_e32 v77, 0x44800000, v33
	v_med3_f32 v75, v73, s64, v72
	v_mul_f32_e32 v67, 0x44800000, v9
	v_mul_f32_e32 v69, 0x44800000, v25
	v_med3_f32 v77, v77, s64, v72
	v_pk_add_f32 v[74:75], v[74:75], s[56:57] op_sel_hi:[1,0]
	v_mul_f32_e32 v66, 0x44800000, v5
	v_med3_f32 v68, v67, s64, v72
	v_mul_f32_e32 v67, 0x44800000, v21
	v_med3_f32 v69, v69, s64, v72
	v_pk_add_f32 v[76:77], v[76:77], s[56:57] op_sel_hi:[1,0]
	v_lshlrev_b32_e32 v73, 16, v75
	v_med3_f32 v66, v66, s64, v72
	v_med3_f32 v67, v67, s64, v72
	v_pk_add_f32 v[68:69], v[68:69], s[56:57] op_sel_hi:[1,0]
	v_and_b32_e32 v73, 0xff0000, v73
	v_lshlrev_b32_e32 v75, 24, v77
	v_pk_add_f32 v[66:67], v[66:67], s[56:57] op_sel_hi:[1,0]
	v_lshlrev_b32_e32 v69, 8, v69
	v_lshlrev_b32_e32 v74, 16, v74
	v_or_b32_e32 v73, v73, v75
	v_and_b32_e32 v69, 0xff00, v69
	v_and_b32_e32 v74, 0xff0000, v74
	v_lshlrev_b32_e32 v76, 24, v76
	v_or_b32_sdwa v67, v73, v67 dst_sel:DWORD dst_unused:UNUSED_PAD src0_sel:DWORD src1_sel:BYTE_0
	v_mul_f32_e32 v73, 0x44800000, v45
	v_or_b32_e32 v74, v74, v76
	v_or_b32_e32 v67, v67, v69
	v_mul_f32_e32 v69, 0x44800000, v41
	v_mul_f32_e32 v75, 0x44800000, v49
	v_med3_f32 v76, v73, s64, v72
	v_mul_f32_e32 v73, 0x44800000, v57
	v_mul_f32_e32 v77, 0x44800000, v61
	v_lshlrev_b32_e32 v68, 8, v68
	v_or_b32_sdwa v66, v74, v66 dst_sel:DWORD dst_unused:UNUSED_PAD src0_sel:DWORD src1_sel:BYTE_0
	v_med3_f32 v74, v69, s64, v72
	v_med3_f32 v78, v75, s64, v72
	v_mul_f32_e32 v79, 0x44800000, v65
	v_med3_f32 v75, v73, s64, v72
	v_med3_f32 v77, v77, s64, v72
	v_and_b32_e32 v68, 0xff00, v68
	v_med3_f32 v79, v79, s64, v72
	v_pk_add_f32 v[74:75], v[74:75], s[56:57] op_sel_hi:[1,0]
	v_pk_add_f32 v[76:77], v[76:77], s[56:57] op_sel_hi:[1,0]
	v_or_b32_e32 v66, v66, v68
	v_mul_f32_e32 v68, 0x44800000, v37
	v_mul_f32_e32 v69, 0x44800000, v53
	v_pk_add_f32 v[78:79], v[78:79], s[56:57] op_sel_hi:[1,0]
	v_lshlrev_b32_e32 v73, 8, v75
	v_lshlrev_b32_e32 v75, 16, v77
	v_lshlrev_b32_e32 v76, 16, v76
	v_med3_f32 v68, v68, s64, v72
	v_med3_f32 v69, v69, s64, v72
	v_and_b32_e32 v75, 0xff0000, v75
	v_and_b32_e32 v76, 0xff0000, v76
	v_lshlrev_b32_e32 v77, 24, v79
	v_lshlrev_b32_e32 v78, 24, v78
	v_pk_add_f32 v[68:69], v[68:69], s[56:57] op_sel_hi:[1,0]
	v_lshlrev_b32_e32 v74, 8, v74
	v_or_b32_e32 v75, v75, v77
	v_or_b32_e32 v76, v76, v78
	v_and_b32_e32 v73, 0xff00, v73
	v_and_b32_e32 v74, 0xff00, v74
	v_or_b32_sdwa v69, v75, v69 dst_sel:DWORD dst_unused:UNUSED_PAD src0_sel:DWORD src1_sel:BYTE_0
	v_or_b32_sdwa v68, v76, v68 dst_sel:DWORD dst_unused:UNUSED_PAD src0_sel:DWORD src1_sel:BYTE_0
	v_or_b32_e32 v69, v69, v73
	v_or_b32_e32 v68, v68, v74
	ds_write_b128 v70, v[66:69] offset:1584
	s_mov_b64 s[28:29], 0

.LBB0_790:
	s_cmp_ge_u32 s17, s16
	v_mov_b32_e32 v66, 0x1690
	s_cbranch_scc1 .LBB0_794
	s_mov_b64 s[30:31], exec
	v_mbcnt_lo_u32_b32 v66, s30, 0
	v_mbcnt_hi_u32_b32 v66, s31, v66
	v_cmp_eq_u32_e32 vcc, 0, v66
	s_and_saveexec_b64 s[28:29], vcc
	s_cbranch_execz .LBB0_793
	s_bcnt1_i32_b64 s11, s[30:31]
	v_mov_b32_e32 v67, s11
	v_mov_b32_e32 v67, v253

.LBB0_1073:
	s_and_saveexec_b64 s[2:3], s[0:1]
	s_cbranch_execz .Lec_2_rest
	v_readlane_b32 s30, v254, 52
	v_readlane_b32 s31, v254, 53
	v_mov_b32_e32 v253, 1
	s_nop 4
	global_atomic_add v253, v71, v253, s[30:31] offset:1280 sc0
.Lec_2_rest:
	s_or_b64 exec, exec, s[2:3]
	v_readlane_b32 s36, v254, 38
	s_mov_b32 s22, s21
	s_mov_b32 s13, s82
	s_mov_b32 s74, s23
	s_mov_b32 s11, s19
	s_mov_b32 s12, s20
	s_mov_b32 s10, s18
	s_mov_b64 s[78:79], s[80:81]
	s_mov_b64 s[30:31], -1
	s_mov_b64 s[2:3], 0
	s_cmp_lt_i32 s21, 2
	s_mov_b64 s[28:29], 0
	v_readlane_b32 s50, v254, 52
	v_readlane_b32 s51, v254, 53
	v_readlane_b32 s37, v254, 39
	v_readlane_b32 s38, v254, 40
	v_readlane_b32 s39, v254, 41
	v_readlane_b32 s40, v254, 42
	v_readlane_b32 s41, v254, 43
	v_readlane_b32 s42, v254, 44
	v_readlane_b32 s43, v254, 45
	v_readlane_b32 s44, v254, 46
	v_readlane_b32 s45, v254, 47
	v_readlane_b32 s46, v254, 48
	v_readlane_b32 s47, v254, 49
	v_readlane_b32 s48, v254, 50
	v_readlane_b32 s49, v254, 51
	s_cbranch_scc1 .LBB0_1080
	s_cmp_eq_u32 s22, 2
	s_mov_b64 s[28:29], -1
	s_cbranch_scc0 .LBB0_1076
	s_waitcnt vmcnt(12)
	v_mul_f32_e32 v70, 0x44800000, v14
	v_mul_f32_e32 v69, 0x44800000, v10
	v_med3_f32 v76, v70, s63, v72
	s_waitcnt vmcnt(9)
	v_mul_f32_e32 v70, 0x44800000, v26
	v_med3_f32 v74, v69, s63, v72
	s_waitcnt vmcnt(8)
	v_mul_f32_e32 v73, 0x44800000, v30
	v_med3_f32 v75, v70, s63, v72
	v_mul_f32_e32 v67, 0x44800000, v6
	v_mul_f32_e32 v69, 0x44800000, v22
	v_med3_f32 v77, v73, s63, v72
	v_pk_add_f32 v[74:75], v[74:75], s[56:57] op_sel_hi:[1,0]
	v_mul_f32_e32 v66, 0x44800000, v2
	v_med3_f32 v68, v67, s63, v72
	v_mul_f32_e32 v67, 0x44800000, v18
	v_med3_f32 v69, v69, s63, v72
	v_pk_add_f32 v[76:77], v[76:77], s[56:57] op_sel_hi:[1,0]
	v_lshlrev_b32_e32 v70, 16, v75
	v_lshlrev_b32_e32 v73, 16, v74
	v_med3_f32 v66, v66, s63, v72
	v_med3_f32 v67, v67, s63, v72
	v_pk_add_f32 v[68:69], v[68:69], s[56:57] op_sel_hi:[1,0]
	v_and_b32_e32 v70, 0xff0000, v70
	v_and_b32_e32 v73, 0xff0000, v73
	v_lshlrev_b32_e32 v74, 24, v77
	v_lshlrev_b32_e32 v75, 24, v76
	v_pk_add_f32 v[66:67], v[66:67], s[56:57] op_sel_hi:[1,0]
	v_lshlrev_b32_e32 v69, 8, v69
	v_or_b32_e32 v70, v70, v74
	v_or_b32_e32 v73, v73, v75
	v_and_b32_e32 v69, 0xff00, v69
	v_or_b32_sdwa v67, v70, v67 dst_sel:DWORD dst_unused:UNUSED_PAD src0_sel:DWORD src1_sel:BYTE_0
	v_or_b32_sdwa v66, v73, v66 dst_sel:DWORD dst_unused:UNUSED_PAD src0_sel:DWORD src1_sel:BYTE_0
	s_waitcnt vmcnt(5)
	v_mul_f32_e32 v70, 0x44800000, v42
	s_waitcnt vmcnt(4)
	v_mul_f32_e32 v73, 0x44800000, v46
	v_or_b32_e32 v67, v67, v69
	v_mul_f32_e32 v69, 0x44800000, v38
	v_med3_f32 v76, v70, s63, v72
	v_med3_f32 v78, v73, s63, v72
	s_waitcnt vmcnt(2)
	v_mul_f32_e32 v70, 0x44800000, v54
	s_waitcnt vmcnt(1)
	v_mul_f32_e32 v73, 0x44800000, v58
	v_lshlrev_b32_e32 v68, 8, v68
	v_med3_f32 v74, v69, s63, v72
	s_waitcnt vmcnt(0)
	v_mul_f32_e32 v79, 0x44800000, v62
	v_med3_f32 v75, v70, s63, v72
	v_med3_f32 v77, v73, s63, v72
	v_and_b32_e32 v68, 0xff00, v68
	v_med3_f32 v79, v79, s63, v72
	v_pk_add_f32 v[74:75], v[74:75], s[56:57] op_sel_hi:[1,0]
	v_pk_add_f32 v[76:77], v[76:77], s[56:57] op_sel_hi:[1,0]
	v_or_b32_e32 v66, v66, v68
	v_mul_f32_e32 v68, 0x44800000, v34
	v_mul_f32_e32 v69, 0x44800000, v50
	v_pk_add_f32 v[78:79], v[78:79], s[56:57] op_sel_hi:[1,0]
	v_lshlrev_b32_e32 v70, 8, v75
	v_lshlrev_b32_e32 v73, 8, v74
	v_lshlrev_b32_e32 v74, 16, v77
	v_lshlrev_b32_e32 v75, 16, v76
	v_med3_f32 v68, v68, s63, v72
	v_med3_f32 v69, v69, s63, v72
	v_and_b32_e32 v74, 0xff0000, v74
	v_and_b32_e32 v75, 0xff0000, v75
	v_lshlrev_b32_e32 v76, 24, v79
	v_lshlrev_b32_e32 v77, 24, v78
	v_pk_add_f32 v[68:69], v[68:69], s[56:57] op_sel_hi:[1,0]
	v_or_b32_e32 v74, v74, v76
	v_or_b32_e32 v75, v75, v77
	v_and_b32_e32 v70, 0xff00, v70
	v_and_b32_e32 v73, 0xff00, v73
	v_or_b32_sdwa v69, v74, v69 dst_sel:DWORD dst_unused:UNUSED_PAD src0_sel:DWORD src1_sel:BYTE_0
	v_or_b32_sdwa v68, v75, v68 dst_sel:DWORD dst_unused:UNUSED_PAD src0_sel:DWORD src1_sel:BYTE_0
	v_or_b32_e32 v69, v69, v70
	v_or_b32_e32 v68, v68, v73
	v_add_u32_e32 v70, v199, v198
	v_mul_f32_e32 v73, 0x44800000, v15
	ds_write_b128 v70, v[66:69]
	v_mul_f32_e32 v69, 0x44800000, v11
	v_med3_f32 v76, v73, s63, v72
	v_mul_f32_e32 v73, 0x44800000, v27
	v_med3_f32 v74, v69, s63, v72
	v_mul_f32_e32 v77, 0x44800000, v31
	v_med3_f32 v75, v73, s63, v72
	v_mul_f32_e32 v67, 0x44800000, v7
	v_mul_f32_e32 v69, 0x44800000, v23
	v_med3_f32 v77, v77, s63, v72
	v_pk_add_f32 v[74:75], v[74:75], s[56:57] op_sel_hi:[1,0]
	v_mul_f32_e32 v66, 0x44800000, v3
	v_med3_f32 v68, v67, s63, v72
	v_mul_f32_e32 v67, 0x44800000, v19
	v_med3_f32 v69, v69, s63, v72
	v_pk_add_f32 v[76:77], v[76:77], s[56:57] op_sel_hi:[1,0]
	v_lshlrev_b32_e32 v73, 16, v75
	v_med3_f32 v66, v66, s63, v72
	v_med3_f32 v67, v67, s63, v72
	v_pk_add_f32 v[68:69], v[68:69], s[56:57] op_sel_hi:[1,0]
	v_and_b32_e32 v73, 0xff0000, v73
	v_lshlrev_b32_e32 v75, 24, v77
	v_pk_add_f32 v[66:67], v[66:67], s[56:57] op_sel_hi:[1,0]
	v_lshlrev_b32_e32 v69, 8, v69
	v_lshlrev_b32_e32 v74, 16, v74
	v_or_b32_e32 v73, v73, v75
	v_and_b32_e32 v69, 0xff00, v69
	v_and_b32_e32 v74, 0xff0000, v74
	v_lshlrev_b32_e32 v76, 24, v76
	v_or_b32_sdwa v67, v73, v67 dst_sel:DWORD dst_unused:UNUSED_PAD src0_sel:DWORD src1_sel:BYTE_0
	v_mul_f32_e32 v73, 0x44800000, v43
	v_or_b32_e32 v74, v74, v76
	v_or_b32_e32 v67, v67, v69
	v_mul_f32_e32 v69, 0x44800000, v39
	v_mul_f32_e32 v75, 0x44800000, v47
	v_med3_f32 v76, v73, s63, v72
	v_mul_f32_e32 v73, 0x44800000, v55
	v_mul_f32_e32 v77, 0x44800000, v59
	v_lshlrev_b32_e32 v68, 8, v68
	v_or_b32_sdwa v66, v74, v66 dst_sel:DWORD dst_unused:UNUSED_PAD src0_sel:DWORD src1_sel:BYTE_0
	v_med3_f32 v74, v69, s63, v72
	v_med3_f32 v78, v75, s63, v72
	v_mul_f32_e32 v79, 0x44800000, v63
	v_med3_f32 v75, v73, s63, v72
	v_med3_f32 v77, v77, s63, v72
	v_and_b32_e32 v68, 0xff00, v68
	v_med3_f32 v79, v79, s63, v72
	v_pk_add_f32 v[74:75], v[74:75], s[56:57] op_sel_hi:[1,0]
	v_pk_add_f32 v[76:77], v[76:77], s[56:57] op_sel_hi:[1,0]
	v_or_b32_e32 v66, v66, v68
	v_mul_f32_e32 v68, 0x44800000, v35
	v_mul_f32_e32 v69, 0x44800000, v51
	v_pk_add_f32 v[78:79], v[78:79], s[56:57] op_sel_hi:[1,0]
	v_lshlrev_b32_e32 v73, 8, v75
	v_lshlrev_b32_e32 v75, 16, v77
	v_lshlrev_b32_e32 v76, 16, v76
	v_med3_f32 v68, v68, s63, v72
	v_med3_f32 v69, v69, s63, v72
	v_and_b32_e32 v75, 0xff0000, v75
	v_and_b32_e32 v76, 0xff0000, v76
	v_lshlrev_b32_e32 v77, 24, v79
	v_lshlrev_b32_e32 v78, 24, v78
	v_pk_add_f32 v[68:69], v[68:69], s[56:57] op_sel_hi:[1,0]
	v_lshlrev_b32_e32 v74, 8, v74
	v_or_b32_e32 v75, v75, v77
	v_or_b32_e32 v76, v76, v78
	v_and_b32_e32 v73, 0xff00, v73
	v_and_b32_e32 v74, 0xff00, v74
	v_or_b32_sdwa v69, v75, v69 dst_sel:DWORD dst_unused:UNUSED_PAD src0_sel:DWORD src1_sel:BYTE_0
	v_or_b32_sdwa v68, v76, v68 dst_sel:DWORD dst_unused:UNUSED_PAD src0_sel:DWORD src1_sel:BYTE_0
	v_or_b32_e32 v69, v69, v73
	v_or_b32_e32 v68, v68, v74
	v_mul_f32_e32 v73, 0x44800000, v16
	ds_write_b128 v70, v[66:69] offset:528
	v_mul_f32_e32 v69, 0x44800000, v12
	v_med3_f32 v76, v73, s63, v72
	v_mul_f32_e32 v73, 0x44800000, v28
	v_med3_f32 v74, v69, s63, v72
	v_mul_f32_e32 v77, 0x44800000, v32
	v_med3_f32 v75, v73, s63, v72
	v_mul_f32_e32 v67, 0x44800000, v8
	v_mul_f32_e32 v69, 0x44800000, v24
	v_med3_f32 v77, v77, s63, v72
	v_pk_add_f32 v[74:75], v[74:75], s[56:57] op_sel_hi:[1,0]
	v_mul_f32_e32 v66, 0x44800000, v4
	v_med3_f32 v68, v67, s63, v72
	v_mul_f32_e32 v67, 0x44800000, v20
	v_med3_f32 v69, v69, s63, v72
	v_pk_add_f32 v[76:77], v[76:77], s[56:57] op_sel_hi:[1,0]
	v_lshlrev_b32_e32 v73, 16, v75
	v_med3_f32 v66, v66, s63, v72
	v_med3_f32 v67, v67, s63, v72
	v_pk_add_f32 v[68:69], v[68:69], s[56:57] op_sel_hi:[1,0]
	v_and_b32_e32 v73, 0xff0000, v73
	v_lshlrev_b32_e32 v75, 24, v77
	v_pk_add_f32 v[66:67], v[66:67], s[56:57] op_sel_hi:[1,0]
	v_lshlrev_b32_e32 v69, 8, v69
	v_lshlrev_b32_e32 v74, 16, v74
	v_or_b32_e32 v73, v73, v75
	v_and_b32_e32 v69, 0xff00, v69
	v_and_b32_e32 v74, 0xff0000, v74
	v_lshlrev_b32_e32 v76, 24, v76
	v_or_b32_sdwa v67, v73, v67 dst_sel:DWORD dst_unused:UNUSED_PAD src0_sel:DWORD src1_sel:BYTE_0
	v_mul_f32_e32 v73, 0x44800000, v44
	v_or_b32_e32 v74, v74, v76
	v_or_b32_e32 v67, v67, v69
	v_mul_f32_e32 v69, 0x44800000, v40
	v_mul_f32_e32 v75, 0x44800000, v48
	v_med3_f32 v76, v73, s63, v72
	v_mul_f32_e32 v73, 0x44800000, v56
	v_mul_f32_e32 v77, 0x44800000, v60
	v_lshlrev_b32_e32 v68, 8, v68
	v_or_b32_sdwa v66, v74, v66 dst_sel:DWORD dst_unused:UNUSED_PAD src0_sel:DWORD src1_sel:BYTE_0
	v_med3_f32 v74, v69, s63, v72
	v_med3_f32 v78, v75, s63, v72
	v_mul_f32_e32 v79, 0x44800000, v64
	v_med3_f32 v75, v73, s63, v72
	v_med3_f32 v77, v77, s63, v72
	v_and_b32_e32 v68, 0xff00, v68
	v_med3_f32 v79, v79, s63, v72
	v_pk_add_f32 v[74:75], v[74:75], s[56:57] op_sel_hi:[1,0]
	v_pk_add_f32 v[76:77], v[76:77], s[56:57] op_sel_hi:[1,0]
	v_or_b32_e32 v66, v66, v68
	v_mul_f32_e32 v68, 0x44800000, v36
	v_mul_f32_e32 v69, 0x44800000, v52
	v_pk_add_f32 v[78:79], v[78:79], s[56:57] op_sel_hi:[1,0]
	v_lshlrev_b32_e32 v73, 8, v75
	v_lshlrev_b32_e32 v75, 16, v77
	v_lshlrev_b32_e32 v76, 16, v76
	v_med3_f32 v68, v68, s63, v72
	v_med3_f32 v69, v69, s63, v72
	v_and_b32_e32 v75, 0xff0000, v75
	v_and_b32_e32 v76, 0xff0000, v76
	v_lshlrev_b32_e32 v77, 24, v79
	v_lshlrev_b32_e32 v78, 24, v78
	v_pk_add_f32 v[68:69], v[68:69], s[56:57] op_sel_hi:[1,0]
	v_lshlrev_b32_e32 v74, 8, v74
	v_or_b32_e32 v75, v75, v77
	v_or_b32_e32 v76, v76, v78
	v_and_b32_e32 v73, 0xff00, v73
	v_and_b32_e32 v74, 0xff00, v74
	v_or_b32_sdwa v69, v75, v69 dst_sel:DWORD dst_unused:UNUSED_PAD src0_sel:DWORD src1_sel:BYTE_0
	v_or_b32_sdwa v68, v76, v68 dst_sel:DWORD dst_unused:UNUSED_PAD src0_sel:DWORD src1_sel:BYTE_0
	v_or_b32_e32 v69, v69, v73
	v_or_b32_e32 v68, v68, v74
	v_mul_f32_e32 v73, 0x44800000, v17
	ds_write_b128 v70, v[66:69] offset:1056
	v_mul_f32_e32 v69, 0x44800000, v13
	v_med3_f32 v76, v73, s63, v72
	v_mul_f32_e32 v73, 0x44800000, v29
	v_med3_f32 v74, v69, s63, v72
	v_mul_f32_e32 v77, 0x44800000, v33
	v_med3_f32 v75, v73, s63, v72
	v_mul_f32_e32 v67, 0x44800000, v9
	v_mul_f32_e32 v69, 0x44800000, v25
	v_med3_f32 v77, v77, s63, v72
	v_pk_add_f32 v[74:75], v[74:75], s[56:57] op_sel_hi:[1,0]
	v_mul_f32_e32 v66, 0x44800000, v5
	v_med3_f32 v68, v67, s63, v72
	v_mul_f32_e32 v67, 0x44800000, v21
	v_med3_f32 v69, v69, s63, v72
	v_pk_add_f32 v[76:77], v[76:77], s[56:57] op_sel_hi:[1,0]
	v_lshlrev_b32_e32 v73, 16, v75
	v_med3_f32 v66, v66, s63, v72
	v_med3_f32 v67, v67, s63, v72
	v_pk_add_f32 v[68:69], v[68:69], s[56:57] op_sel_hi:[1,0]
	v_and_b32_e32 v73, 0xff0000, v73
	v_lshlrev_b32_e32 v75, 24, v77
	v_pk_add_f32 v[66:67], v[66:67], s[56:57] op_sel_hi:[1,0]
	v_lshlrev_b32_e32 v69, 8, v69
	v_lshlrev_b32_e32 v74, 16, v74
	v_or_b32_e32 v73, v73, v75
	v_and_b32_e32 v69, 0xff00, v69
	v_and_b32_e32 v74, 0xff0000, v74
	v_lshlrev_b32_e32 v76, 24, v76
	v_or_b32_sdwa v67, v73, v67 dst_sel:DWORD dst_unused:UNUSED_PAD src0_sel:DWORD src1_sel:BYTE_0
	v_mul_f32_e32 v73, 0x44800000, v45
	v_or_b32_e32 v74, v74, v76
	v_or_b32_e32 v67, v67, v69
	v_mul_f32_e32 v69, 0x44800000, v41
	v_mul_f32_e32 v75, 0x44800000, v49
	v_med3_f32 v76, v73, s63, v72
	v_mul_f32_e32 v73, 0x44800000, v57
	v_mul_f32_e32 v77, 0x44800000, v61
	v_lshlrev_b32_e32 v68, 8, v68
	v_or_b32_sdwa v66, v74, v66 dst_sel:DWORD dst_unused:UNUSED_PAD src0_sel:DWORD src1_sel:BYTE_0
	v_med3_f32 v74, v69, s63, v72
	v_med3_f32 v78, v75, s63, v72
	v_mul_f32_e32 v79, 0x44800000, v65
	v_med3_f32 v75, v73, s63, v72
	v_med3_f32 v77, v77, s63, v72
	v_and_b32_e32 v68, 0xff00, v68
	v_med3_f32 v79, v79, s63, v72
	v_pk_add_f32 v[74:75], v[74:75], s[56:57] op_sel_hi:[1,0]
	v_pk_add_f32 v[76:77], v[76:77], s[56:57] op_sel_hi:[1,0]
	v_or_b32_e32 v66, v66, v68
	v_mul_f32_e32 v68, 0x44800000, v37
	v_mul_f32_e32 v69, 0x44800000, v53
	v_pk_add_f32 v[78:79], v[78:79], s[56:57] op_sel_hi:[1,0]
	v_lshlrev_b32_e32 v73, 8, v75
	v_lshlrev_b32_e32 v75, 16, v77
	v_lshlrev_b32_e32 v76, 16, v76
	v_med3_f32 v68, v68, s63, v72
	v_med3_f32 v69, v69, s63, v72
	v_and_b32_e32 v75, 0xff0000, v75
	v_and_b32_e32 v76, 0xff0000, v76
	v_lshlrev_b32_e32 v77, 24, v79
	v_lshlrev_b32_e32 v78, 24, v78
	v_pk_add_f32 v[68:69], v[68:69], s[56:57] op_sel_hi:[1,0]
	v_lshlrev_b32_e32 v74, 8, v74
	v_or_b32_e32 v75, v75, v77
	v_or_b32_e32 v76, v76, v78
	v_and_b32_e32 v73, 0xff00, v73
	v_and_b32_e32 v74, 0xff00, v74
	v_or_b32_sdwa v69, v75, v69 dst_sel:DWORD dst_unused:UNUSED_PAD src0_sel:DWORD src1_sel:BYTE_0
	v_or_b32_sdwa v68, v76, v68 dst_sel:DWORD dst_unused:UNUSED_PAD src0_sel:DWORD src1_sel:BYTE_0
	v_or_b32_e32 v69, v69, v73
	v_or_b32_e32 v68, v68, v74
	ds_write_b128 v70, v[66:69] offset:1584
	s_mov_b64 s[28:29], 0

.LBB0_1084:
	s_cmp_eq_u32 s62, 0
	s_cbranch_scc1 .LBB0_1088
	s_mov_b64 s[30:31], exec
	v_mbcnt_lo_u32_b32 v66, s30, 0
	v_mbcnt_hi_u32_b32 v66, s31, v66
	v_cmp_eq_u32_e32 vcc, 0, v66
	s_and_saveexec_b64 s[28:29], vcc
	s_cbranch_execz .LBB0_1087
	s_bcnt1_i32_b64 s18, s[30:31]
	v_mov_b32_e32 v67, s18
	v_mov_b32_e32 v67, v253

.LBB0_2106:
	s_cmp_gt_u32 s17, 20
	s_cbranch_scc1 .Lec_3_skip
	s_and_saveexec_b64 s[2:3], s[0:1]
	s_cbranch_execz .Lec_3_rest
	v_readlane_b32 s30, v254, 52
	v_readlane_b32 s31, v254, 53
	v_mov_b32_e32 v253, 1
	s_nop 4
	global_atomic_add v253, v75, v253, s[30:31] offset:1536 sc0
.Lec_3_rest:
	s_or_b64 exec, exec, s[2:3]
.Lec_3_skip:
	s_mov_b32 s69, s25
	s_mov_b32 s19, s80
	s_mov_b32 s68, s83
	s_mov_b32 s11, s23
	s_mov_b32 s18, s24
	s_mov_b32 s10, s22
	s_mov_b64 s[76:77], s[78:79]
	s_mov_b64 s[30:31], -1
	s_mov_b64 s[2:3], 0
	s_cmp_lt_i32 s25, 2
	s_mov_b64 s[28:29], 0
	s_cbranch_scc1 .LBB0_2113
	s_cmp_eq_u32 s69, 2
	s_mov_b64 s[28:29], -1
	s_cbranch_scc0 .LBB0_2109
	s_waitcnt vmcnt(12)
	v_mul_f32_e32 v74, 0x44800000, v14
	v_mul_f32_e32 v69, 0x44800000, v10
	v_med3_f32 v86, v74, s67, v71
	s_waitcnt vmcnt(9)
	v_mul_f32_e32 v74, 0x44800000, v26
	v_med3_f32 v84, v69, s67, v71
	s_waitcnt vmcnt(8)
	v_mul_f32_e32 v77, 0x44800000, v30
	v_med3_f32 v85, v74, s67, v71
	v_mul_f32_e32 v67, 0x44800000, v6
	v_med3_f32 v87, v77, s67, v71
	v_pk_add_f32 v[84:85], v[84:85], s[26:27] op_sel_hi:[1,0]
	v_mul_f32_e32 v66, 0x44800000, v2
	v_med3_f32 v68, v67, s67, v71
	v_mul_f32_e32 v67, 0x44800000, v18
	v_mul_f32_e32 v69, 0x44800000, v22
	v_pk_add_f32 v[86:87], v[86:87], s[26:27] op_sel_hi:[1,0]
	v_lshlrev_b32_e32 v77, 16, v84
	v_med3_f32 v66, v66, s67, v71
	v_med3_f32 v67, v67, s67, v71
	v_med3_f32 v69, v69, s67, v71
	v_lshlrev_b32_e32 v74, 16, v85
	v_and_b32_e32 v77, 0xff0000, v77
	v_lshlrev_b32_e32 v83, 24, v86
	v_pk_add_f32 v[66:67], v[66:67], s[26:27] op_sel_hi:[1,0]
	v_pk_add_f32 v[68:69], v[68:69], s[26:27] op_sel_hi:[1,0]
	v_and_b32_e32 v74, 0xff0000, v74
	v_lshlrev_b32_e32 v79, 24, v87
	v_or_b32_e32 v77, v77, v83
	v_lshlrev_b32_e32 v69, 8, v69
	v_or_b32_e32 v74, v74, v79
	v_or_b32_sdwa v66, v77, v66 dst_sel:DWORD dst_unused:UNUSED_PAD src0_sel:DWORD src1_sel:BYTE_0
	s_waitcnt vmcnt(4)
	v_mul_f32_e32 v77, 0x44800000, v46
	v_and_b32_e32 v69, 0xff00, v69
	v_or_b32_sdwa v67, v74, v67 dst_sel:DWORD dst_unused:UNUSED_PAD src0_sel:DWORD src1_sel:BYTE_0
	v_mul_f32_e32 v74, 0x44800000, v42
	v_med3_f32 v88, v77, s67, v71
	s_waitcnt vmcnt(1)
	v_mul_f32_e32 v77, 0x44800000, v58
	v_lshlrev_b32_e32 v68, 8, v68
	v_or_b32_e32 v67, v67, v69
	v_mul_f32_e32 v69, 0x44800000, v38
	v_med3_f32 v86, v74, s67, v71
	v_mul_f32_e32 v74, 0x44800000, v54
	s_waitcnt vmcnt(0)
	v_mul_f32_e32 v79, 0x44800000, v62
	v_med3_f32 v87, v77, s67, v71
	v_and_b32_e32 v68, 0xff00, v68
	v_med3_f32 v84, v69, s67, v71
	v_med3_f32 v85, v74, s67, v71
	v_med3_f32 v89, v79, s67, v71
	v_pk_add_f32 v[86:87], v[86:87], s[26:27] op_sel_hi:[1,0]
	v_or_b32_e32 v66, v66, v68
	v_mul_f32_e32 v68, 0x44800000, v34
	v_mul_f32_e32 v69, 0x44800000, v50
	v_pk_add_f32 v[84:85], v[84:85], s[26:27] op_sel_hi:[1,0]
	v_pk_add_f32 v[88:89], v[88:89], s[26:27] op_sel_hi:[1,0]
	v_lshlrev_b32_e32 v79, 16, v87
	v_lshlrev_b32_e32 v83, 16, v86
	v_med3_f32 v68, v68, s67, v71
	v_med3_f32 v69, v69, s67, v71
	v_lshlrev_b32_e32 v74, 8, v85
	v_lshlrev_b32_e32 v77, 8, v84
	v_and_b32_e32 v79, 0xff0000, v79
	v_and_b32_e32 v83, 0xff0000, v83
	v_lshlrev_b32_e32 v84, 24, v89
	v_lshlrev_b32_e32 v85, 24, v88
	v_pk_add_f32 v[68:69], v[68:69], s[26:27] op_sel_hi:[1,0]
	v_or_b32_e32 v79, v79, v84
	v_or_b32_e32 v83, v83, v85
	v_and_b32_e32 v74, 0xff00, v74
	v_and_b32_e32 v77, 0xff00, v77
	v_or_b32_sdwa v69, v79, v69 dst_sel:DWORD dst_unused:UNUSED_PAD src0_sel:DWORD src1_sel:BYTE_0
	v_or_b32_sdwa v68, v83, v68 dst_sel:DWORD dst_unused:UNUSED_PAD src0_sel:DWORD src1_sel:BYTE_0
	v_or_b32_e32 v69, v69, v74
	v_or_b32_e32 v68, v68, v77
	v_add_u32_e32 v74, v199, v198
	v_mul_f32_e32 v77, 0x44800000, v15
	ds_write_b128 v74, v[66:69]
	v_mul_f32_e32 v69, 0x44800000, v11
	v_med3_f32 v86, v77, s67, v71
	v_mul_f32_e32 v77, 0x44800000, v27
	v_med3_f32 v84, v69, s67, v71
	v_mul_f32_e32 v79, 0x44800000, v31
	v_med3_f32 v85, v77, s67, v71
	v_mul_f32_e32 v67, 0x44800000, v7
	v_mul_f32_e32 v69, 0x44800000, v23
	v_med3_f32 v87, v79, s67, v71
	v_pk_add_f32 v[84:85], v[84:85], s[26:27] op_sel_hi:[1,0]
	v_mul_f32_e32 v66, 0x44800000, v3
	v_med3_f32 v68, v67, s67, v71
	v_mul_f32_e32 v67, 0x44800000, v19
	v_med3_f32 v69, v69, s67, v71
	v_pk_add_f32 v[86:87], v[86:87], s[26:27] op_sel_hi:[1,0]
	v_lshlrev_b32_e32 v77, 16, v85
	v_lshlrev_b32_e32 v79, 16, v84
	v_med3_f32 v66, v66, s67, v71
	v_med3_f32 v67, v67, s67, v71
	v_pk_add_f32 v[68:69], v[68:69], s[26:27] op_sel_hi:[1,0]
	v_and_b32_e32 v77, 0xff0000, v77
	v_and_b32_e32 v79, 0xff0000, v79
	v_lshlrev_b32_e32 v83, 24, v87
	v_lshlrev_b32_e32 v84, 24, v86
	v_pk_add_f32 v[66:67], v[66:67], s[26:27] op_sel_hi:[1,0]
	v_lshlrev_b32_e32 v69, 8, v69
	v_or_b32_e32 v77, v77, v83
	v_or_b32_e32 v79, v79, v84
	v_and_b32_e32 v69, 0xff00, v69
	v_or_b32_sdwa v67, v77, v67 dst_sel:DWORD dst_unused:UNUSED_PAD src0_sel:DWORD src1_sel:BYTE_0
	v_or_b32_sdwa v66, v79, v66 dst_sel:DWORD dst_unused:UNUSED_PAD src0_sel:DWORD src1_sel:BYTE_0
	v_mul_f32_e32 v77, 0x44800000, v43
	v_mul_f32_e32 v79, 0x44800000, v47
	v_or_b32_e32 v67, v67, v69
	v_mul_f32_e32 v69, 0x44800000, v39
	v_med3_f32 v86, v77, s67, v71
	v_med3_f32 v88, v79, s67, v71
	v_mul_f32_e32 v77, 0x44800000, v55
	v_mul_f32_e32 v79, 0x44800000, v59
	v_lshlrev_b32_e32 v68, 8, v68
	v_med3_f32 v84, v69, s67, v71
	v_mul_f32_e32 v83, 0x44800000, v63
	v_med3_f32 v85, v77, s67, v71
	v_med3_f32 v87, v79, s67, v71
	v_and_b32_e32 v68, 0xff00, v68
	v_med3_f32 v89, v83, s67, v71
	v_pk_add_f32 v[84:85], v[84:85], s[26:27] op_sel_hi:[1,0]
	v_pk_add_f32 v[86:87], v[86:87], s[26:27] op_sel_hi:[1,0]
	v_or_b32_e32 v66, v66, v68
	v_mul_f32_e32 v68, 0x44800000, v35
	v_mul_f32_e32 v69, 0x44800000, v51
	v_pk_add_f32 v[88:89], v[88:89], s[26:27] op_sel_hi:[1,0]
	v_lshlrev_b32_e32 v79, 8, v84
	v_lshlrev_b32_e32 v83, 16, v87
	v_lshlrev_b32_e32 v84, 16, v86
	v_med3_f32 v68, v68, s67, v71
	v_med3_f32 v69, v69, s67, v71
	v_lshlrev_b32_e32 v77, 8, v85
	v_and_b32_e32 v83, 0xff0000, v83
	v_and_b32_e32 v84, 0xff0000, v84
	v_lshlrev_b32_e32 v85, 24, v89
	v_lshlrev_b32_e32 v86, 24, v88
	v_pk_add_f32 v[68:69], v[68:69], s[26:27] op_sel_hi:[1,0]
	v_or_b32_e32 v83, v83, v85
	v_or_b32_e32 v84, v84, v86
	v_and_b32_e32 v77, 0xff00, v77
	v_and_b32_e32 v79, 0xff00, v79
	v_or_b32_sdwa v69, v83, v69 dst_sel:DWORD dst_unused:UNUSED_PAD src0_sel:DWORD src1_sel:BYTE_0
	v_or_b32_sdwa v68, v84, v68 dst_sel:DWORD dst_unused:UNUSED_PAD src0_sel:DWORD src1_sel:BYTE_0
	v_or_b32_e32 v69, v69, v77
	v_or_b32_e32 v68, v68, v79
	v_mul_f32_e32 v77, 0x44800000, v16
	ds_write_b128 v74, v[66:69] offset:528
	v_mul_f32_e32 v69, 0x44800000, v12
	v_med3_f32 v86, v77, s67, v71
	v_mul_f32_e32 v77, 0x44800000, v28
	v_med3_f32 v84, v69, s67, v71
	v_mul_f32_e32 v79, 0x44800000, v32
	v_med3_f32 v85, v77, s67, v71
	v_mul_f32_e32 v67, 0x44800000, v8
	v_mul_f32_e32 v69, 0x44800000, v24
	v_med3_f32 v87, v79, s67, v71
	v_pk_add_f32 v[84:85], v[84:85], s[26:27] op_sel_hi:[1,0]
	v_mul_f32_e32 v66, 0x44800000, v4
	v_med3_f32 v68, v67, s67, v71
	v_mul_f32_e32 v67, 0x44800000, v20
	v_med3_f32 v69, v69, s67, v71
	v_pk_add_f32 v[86:87], v[86:87], s[26:27] op_sel_hi:[1,0]
	v_lshlrev_b32_e32 v77, 16, v85
	v_lshlrev_b32_e32 v79, 16, v84
	v_med3_f32 v66, v66, s67, v71
	v_med3_f32 v67, v67, s67, v71
	v_pk_add_f32 v[68:69], v[68:69], s[26:27] op_sel_hi:[1,0]
	v_and_b32_e32 v77, 0xff0000, v77
	v_and_b32_e32 v79, 0xff0000, v79
	v_lshlrev_b32_e32 v83, 24, v87
	v_lshlrev_b32_e32 v84, 24, v86
	v_pk_add_f32 v[66:67], v[66:67], s[26:27] op_sel_hi:[1,0]
	v_lshlrev_b32_e32 v69, 8, v69
	v_or_b32_e32 v77, v77, v83
	v_or_b32_e32 v79, v79, v84
	v_and_b32_e32 v69, 0xff00, v69
	v_or_b32_sdwa v67, v77, v67 dst_sel:DWORD dst_unused:UNUSED_PAD src0_sel:DWORD src1_sel:BYTE_0
	v_or_b32_sdwa v66, v79, v66 dst_sel:DWORD dst_unused:UNUSED_PAD src0_sel:DWORD src1_sel:BYTE_0
	v_mul_f32_e32 v77, 0x44800000, v44
	v_mul_f32_e32 v79, 0x44800000, v48
	v_or_b32_e32 v67, v67, v69
	v_mul_f32_e32 v69, 0x44800000, v40
	v_med3_f32 v86, v77, s67, v71
	v_med3_f32 v88, v79, s67, v71
	v_mul_f32_e32 v77, 0x44800000, v56
	v_mul_f32_e32 v79, 0x44800000, v60
	v_lshlrev_b32_e32 v68, 8, v68
	v_med3_f32 v84, v69, s67, v71
	v_mul_f32_e32 v83, 0x44800000, v64
	v_med3_f32 v85, v77, s67, v71
	v_med3_f32 v87, v79, s67, v71
	v_and_b32_e32 v68, 0xff00, v68
	v_med3_f32 v89, v83, s67, v71
	v_pk_add_f32 v[84:85], v[84:85], s[26:27] op_sel_hi:[1,0]
	v_pk_add_f32 v[86:87], v[86:87], s[26:27] op_sel_hi:[1,0]
	v_or_b32_e32 v66, v66, v68
	v_mul_f32_e32 v68, 0x44800000, v36
	v_mul_f32_e32 v69, 0x44800000, v52
	v_pk_add_f32 v[88:89], v[88:89], s[26:27] op_sel_hi:[1,0]
	v_lshlrev_b32_e32 v79, 8, v84
	v_lshlrev_b32_e32 v83, 16, v87
	v_lshlrev_b32_e32 v84, 16, v86
	v_med3_f32 v68, v68, s67, v71
	v_med3_f32 v69, v69, s67, v71
	v_lshlrev_b32_e32 v77, 8, v85
	v_and_b32_e32 v83, 0xff0000, v83
	v_and_b32_e32 v84, 0xff0000, v84
	v_lshlrev_b32_e32 v85, 24, v89
	v_lshlrev_b32_e32 v86, 24, v88
	v_pk_add_f32 v[68:69], v[68:69], s[26:27] op_sel_hi:[1,0]
	v_or_b32_e32 v83, v83, v85
	v_or_b32_e32 v84, v84, v86
	v_and_b32_e32 v77, 0xff00, v77
	v_and_b32_e32 v79, 0xff00, v79
	v_or_b32_sdwa v69, v83, v69 dst_sel:DWORD dst_unused:UNUSED_PAD src0_sel:DWORD src1_sel:BYTE_0
	v_or_b32_sdwa v68, v84, v68 dst_sel:DWORD dst_unused:UNUSED_PAD src0_sel:DWORD src1_sel:BYTE_0
	v_or_b32_e32 v69, v69, v77
	v_or_b32_e32 v68, v68, v79
	v_mul_f32_e32 v77, 0x44800000, v17
	ds_write_b128 v74, v[66:69] offset:1056
	v_mul_f32_e32 v69, 0x44800000, v13
	v_med3_f32 v86, v77, s67, v71
	v_mul_f32_e32 v77, 0x44800000, v29
	v_med3_f32 v84, v69, s67, v71
	v_mul_f32_e32 v79, 0x44800000, v33
	v_med3_f32 v85, v77, s67, v71
	v_mul_f32_e32 v67, 0x44800000, v9
	v_mul_f32_e32 v69, 0x44800000, v25
	v_med3_f32 v87, v79, s67, v71
	v_pk_add_f32 v[84:85], v[84:85], s[26:27] op_sel_hi:[1,0]
	v_mul_f32_e32 v66, 0x44800000, v5
	v_med3_f32 v68, v67, s67, v71
	v_mul_f32_e32 v67, 0x44800000, v21
	v_med3_f32 v69, v69, s67, v71
	v_pk_add_f32 v[86:87], v[86:87], s[26:27] op_sel_hi:[1,0]
	v_lshlrev_b32_e32 v77, 16, v85
	v_lshlrev_b32_e32 v79, 16, v84
	v_med3_f32 v66, v66, s67, v71
	v_med3_f32 v67, v67, s67, v71
	v_pk_add_f32 v[68:69], v[68:69], s[26:27] op_sel_hi:[1,0]
	v_and_b32_e32 v77, 0xff0000, v77
	v_and_b32_e32 v79, 0xff0000, v79
	v_lshlrev_b32_e32 v83, 24, v87
	v_lshlrev_b32_e32 v84, 24, v86
	v_pk_add_f32 v[66:67], v[66:67], s[26:27] op_sel_hi:[1,0]
	v_lshlrev_b32_e32 v69, 8, v69
	v_or_b32_e32 v77, v77, v83
	v_or_b32_e32 v79, v79, v84
	v_and_b32_e32 v69, 0xff00, v69
	v_or_b32_sdwa v67, v77, v67 dst_sel:DWORD dst_unused:UNUSED_PAD src0_sel:DWORD src1_sel:BYTE_0
	v_or_b32_sdwa v66, v79, v66 dst_sel:DWORD dst_unused:UNUSED_PAD src0_sel:DWORD src1_sel:BYTE_0
	v_mul_f32_e32 v77, 0x44800000, v45
	v_mul_f32_e32 v79, 0x44800000, v49
	v_or_b32_e32 v67, v67, v69
	v_mul_f32_e32 v69, 0x44800000, v41
	v_med3_f32 v86, v77, s67, v71
	v_med3_f32 v88, v79, s67, v71
	v_mul_f32_e32 v77, 0x44800000, v57
	v_mul_f32_e32 v79, 0x44800000, v61
	v_lshlrev_b32_e32 v68, 8, v68
	v_med3_f32 v84, v69, s67, v71
	v_mul_f32_e32 v83, 0x44800000, v65
	v_med3_f32 v85, v77, s67, v71
	v_med3_f32 v87, v79, s67, v71
	v_and_b32_e32 v68, 0xff00, v68
	v_med3_f32 v89, v83, s67, v71
	v_pk_add_f32 v[84:85], v[84:85], s[26:27] op_sel_hi:[1,0]
	v_pk_add_f32 v[86:87], v[86:87], s[26:27] op_sel_hi:[1,0]
	v_or_b32_e32 v66, v66, v68
	v_mul_f32_e32 v68, 0x44800000, v37
	v_mul_f32_e32 v69, 0x44800000, v53
	v_pk_add_f32 v[88:89], v[88:89], s[26:27] op_sel_hi:[1,0]
	v_lshlrev_b32_e32 v79, 8, v84
	v_lshlrev_b32_e32 v83, 16, v87
	v_lshlrev_b32_e32 v84, 16, v86
	v_med3_f32 v68, v68, s67, v71
	v_med3_f32 v69, v69, s67, v71
	v_lshlrev_b32_e32 v77, 8, v85
	v_and_b32_e32 v83, 0xff0000, v83
	v_and_b32_e32 v84, 0xff0000, v84
	v_lshlrev_b32_e32 v85, 24, v89
	v_lshlrev_b32_e32 v86, 24, v88
	v_pk_add_f32 v[68:69], v[68:69], s[26:27] op_sel_hi:[1,0]
	v_or_b32_e32 v83, v83, v85
	v_or_b32_e32 v84, v84, v86
	v_and_b32_e32 v77, 0xff00, v77
	v_and_b32_e32 v79, 0xff00, v79
	v_or_b32_sdwa v69, v83, v69 dst_sel:DWORD dst_unused:UNUSED_PAD src0_sel:DWORD src1_sel:BYTE_0
	v_or_b32_sdwa v68, v84, v68 dst_sel:DWORD dst_unused:UNUSED_PAD src0_sel:DWORD src1_sel:BYTE_0
	v_or_b32_e32 v69, v69, v77
	v_or_b32_e32 v68, v68, v79
	ds_write_b128 v74, v[66:69] offset:1584
	s_mov_b64 s[28:29], 0

.LBB0_2117:
	s_cmp_gt_u32 s17, 20
	v_mov_b32_e32 v66, 0x26a0
	s_cbranch_scc1 .LBB0_2121
	s_mov_b64 s[30:31], exec
	v_mbcnt_lo_u32_b32 v66, s30, 0
	v_mbcnt_hi_u32_b32 v66, s31, v66
	v_cmp_eq_u32_e32 vcc, 0, v66
	s_and_saveexec_b64 s[28:29], vcc
	s_cbranch_execz .LBB0_2120
	s_bcnt1_i32_b64 s22, s[30:31]
	v_readlane_b32 s36, v254, 38
	v_mov_b32_e32 v67, s22
	v_readlane_b32 s50, v254, 52
	v_readlane_b32 s51, v254, 53
	v_readlane_b32 s37, v254, 39
	v_readlane_b32 s38, v254, 40
	v_readlane_b32 s39, v254, 41
	v_readlane_b32 s40, v254, 42
	v_readlane_b32 s41, v254, 43
	v_mov_b32_e32 v67, v253
	v_readlane_b32 s42, v254, 44
	v_readlane_b32 s43, v254, 45
	v_readlane_b32 s44, v254, 46
	v_readlane_b32 s45, v254, 47
	v_readlane_b32 s46, v254, 48
	v_readlane_b32 s47, v254, 49
	v_readlane_b32 s48, v254, 50
	v_readlane_b32 s49, v254, 51

.LBB0_2292:
	s_cmpk_lt_i32 s8, 0x80
	s_cselect_b32 s6, 1, 0
	s_and_b64 s[2:3], s[4:5], exec
	s_cselect_b32 s33, s6, 4
	s_cmp_lg_u32 s33, 0
	v_mov_b32_e32 v206, v205
	v_mov_b32_e32 v207, v213
	v_mov_b32_e32 v213, v209
	v_mov_b32_e32 v209, v211
	v_or_b32_e32 v211, 0x60, v1
	s_waitcnt lgkmcnt(0)
	s_barrier
	s_cbranch_scc0 .LBB0_2499
	s_and_saveexec_b64 s[2:3], s[0:1]
	s_cbranch_execz .LBB0_2297
	s_mov_b64 s[6:7], exec
	s_waitcnt vmcnt(15)
	v_mbcnt_lo_u32_b32 v2, s6, 0
	v_mbcnt_hi_u32_b32 v2, s7, v2
	v_cmp_eq_u32_e32 vcc, 0, v2
	s_and_saveexec_b64 s[4:5], vcc
	s_cbranch_execz .LBB0_2296
	s_bcnt1_i32_b64 s6, s[6:7]
	v_mov_b32_e32 v3, 0
	v_mov_b32_e32 v4, s6
	global_atomic_add v3, v3, v4, s[94:95] offset:1536 sc0

.LBB0_2347:
	s_cmp_ge_u32 s17, s33
	s_cbranch_scc1 .Lec_4_skip
	s_and_saveexec_b64 s[2:3], s[0:1]
	s_cbranch_execz .Lec_4_rest
	v_mov_b32_e32 v253, 1
	global_atomic_add v253, v71, v253, s[94:95] offset:1536 sc0
.Lec_4_rest:
	s_or_b64 exec, exec, s[2:3]
.Lec_4_skip:
	s_mov_b32 s21, s77
	s_mov_b32 s23, s54
	s_mov_b32 s20, s78
	s_mov_b32 s11, s25
	s_mov_b32 s22, s76
	s_mov_b32 s10, s24
	s_mov_b64 s[26:27], s[52:53]
	s_mov_b64 s[30:31], -1
	s_mov_b64 s[2:3], 0
	s_cmp_lt_i32 s77, 2
	s_mov_b64 s[28:29], 0
	s_cbranch_scc1 .LBB0_2354
	s_cmp_eq_u32 s21, 2
	s_mov_b64 s[28:29], -1
	s_cbranch_scc0 .LBB0_2350
	s_waitcnt vmcnt(12)
	v_mul_f32_e32 v70, 0x44800000, v14
	v_mul_f32_e32 v69, 0x44800000, v10
	v_med3_f32 v76, v70, s70, v72
	s_waitcnt vmcnt(9)
	v_mul_f32_e32 v70, 0x44800000, v26
	v_med3_f32 v74, v69, s70, v72
	s_waitcnt vmcnt(8)
	v_mul_f32_e32 v73, 0x44800000, v30
	v_med3_f32 v75, v70, s70, v72
	v_mul_f32_e32 v67, 0x44800000, v6
	v_mul_f32_e32 v69, 0x44800000, v22
	v_med3_f32 v77, v73, s70, v72
	v_pk_add_f32 v[74:75], v[74:75], s[16:17] op_sel_hi:[1,0]
	v_mul_f32_e32 v66, 0x44800000, v2
	v_med3_f32 v68, v67, s70, v72
	v_mul_f32_e32 v67, 0x44800000, v18
	v_med3_f32 v69, v69, s70, v72
	v_pk_add_f32 v[76:77], v[76:77], s[16:17] op_sel_hi:[1,0]
	v_lshlrev_b32_e32 v70, 16, v75
	v_lshlrev_b32_e32 v73, 16, v74
	v_med3_f32 v66, v66, s70, v72
	v_med3_f32 v67, v67, s70, v72
	v_pk_add_f32 v[68:69], v[68:69], s[16:17] op_sel_hi:[1,0]
	v_and_b32_e32 v70, 0xff0000, v70
	v_and_b32_e32 v73, 0xff0000, v73
	v_lshlrev_b32_e32 v74, 24, v77
	v_lshlrev_b32_e32 v75, 24, v76
	v_pk_add_f32 v[66:67], v[66:67], s[16:17] op_sel_hi:[1,0]
	v_lshlrev_b32_e32 v69, 8, v69
	v_or_b32_e32 v70, v70, v74
	v_or_b32_e32 v73, v73, v75
	v_and_b32_e32 v69, 0xff00, v69
	v_or_b32_sdwa v67, v70, v67 dst_sel:DWORD dst_unused:UNUSED_PAD src0_sel:DWORD src1_sel:BYTE_0
	v_or_b32_sdwa v66, v73, v66 dst_sel:DWORD dst_unused:UNUSED_PAD src0_sel:DWORD src1_sel:BYTE_0
	s_waitcnt vmcnt(5)
	v_mul_f32_e32 v70, 0x44800000, v42
	s_waitcnt vmcnt(4)
	v_mul_f32_e32 v73, 0x44800000, v46
	v_or_b32_e32 v67, v67, v69
	v_mul_f32_e32 v69, 0x44800000, v38
	v_med3_f32 v76, v70, s70, v72
	v_med3_f32 v78, v73, s70, v72
	s_waitcnt vmcnt(2)
	v_mul_f32_e32 v70, 0x44800000, v54
	s_waitcnt vmcnt(1)
	v_mul_f32_e32 v73, 0x44800000, v58
	v_lshlrev_b32_e32 v68, 8, v68
	v_med3_f32 v74, v69, s70, v72
	s_waitcnt vmcnt(0)
	v_mul_f32_e32 v79, 0x44800000, v62
	v_med3_f32 v75, v70, s70, v72
	v_med3_f32 v77, v73, s70, v72
	v_and_b32_e32 v68, 0xff00, v68
	v_med3_f32 v79, v79, s70, v72
	v_pk_add_f32 v[74:75], v[74:75], s[16:17] op_sel_hi:[1,0]
	v_pk_add_f32 v[76:77], v[76:77], s[16:17] op_sel_hi:[1,0]
	v_or_b32_e32 v66, v66, v68
	v_mul_f32_e32 v68, 0x44800000, v34
	v_mul_f32_e32 v69, 0x44800000, v50
	v_pk_add_f32 v[78:79], v[78:79], s[16:17] op_sel_hi:[1,0]
	v_lshlrev_b32_e32 v70, 8, v75
	v_lshlrev_b32_e32 v73, 8, v74
	v_lshlrev_b32_e32 v74, 16, v77
	v_lshlrev_b32_e32 v75, 16, v76
	v_med3_f32 v68, v68, s70, v72
	v_med3_f32 v69, v69, s70, v72
	v_and_b32_e32 v74, 0xff0000, v74
	v_and_b32_e32 v75, 0xff0000, v75
	v_lshlrev_b32_e32 v76, 24, v79
	v_lshlrev_b32_e32 v77, 24, v78
	v_pk_add_f32 v[68:69], v[68:69], s[16:17] op_sel_hi:[1,0]
	v_or_b32_e32 v74, v74, v76
	v_or_b32_e32 v75, v75, v77
	v_and_b32_e32 v70, 0xff00, v70
	v_and_b32_e32 v73, 0xff00, v73
	v_or_b32_sdwa v69, v74, v69 dst_sel:DWORD dst_unused:UNUSED_PAD src0_sel:DWORD src1_sel:BYTE_0
	v_or_b32_sdwa v68, v75, v68 dst_sel:DWORD dst_unused:UNUSED_PAD src0_sel:DWORD src1_sel:BYTE_0
	v_or_b32_e32 v69, v69, v70
	v_or_b32_e32 v68, v68, v73
	v_add_u32_e32 v70, v199, v198
	v_mul_f32_e32 v73, 0x44800000, v15
	ds_write_b128 v70, v[66:69]
	v_mul_f32_e32 v69, 0x44800000, v11
	v_med3_f32 v76, v73, s70, v72
	v_mul_f32_e32 v73, 0x44800000, v27
	v_med3_f32 v74, v69, s70, v72
	v_mul_f32_e32 v77, 0x44800000, v31
	v_med3_f32 v75, v73, s70, v72
	v_mul_f32_e32 v67, 0x44800000, v7
	v_mul_f32_e32 v69, 0x44800000, v23
	v_med3_f32 v77, v77, s70, v72
	v_pk_add_f32 v[74:75], v[74:75], s[16:17] op_sel_hi:[1,0]
	v_mul_f32_e32 v66, 0x44800000, v3
	v_med3_f32 v68, v67, s70, v72
	v_mul_f32_e32 v67, 0x44800000, v19
	v_med3_f32 v69, v69, s70, v72
	v_pk_add_f32 v[76:77], v[76:77], s[16:17] op_sel_hi:[1,0]
	v_lshlrev_b32_e32 v73, 16, v75
	v_med3_f32 v66, v66, s70, v72
	v_med3_f32 v67, v67, s70, v72
	v_pk_add_f32 v[68:69], v[68:69], s[16:17] op_sel_hi:[1,0]
	v_and_b32_e32 v73, 0xff0000, v73
	v_lshlrev_b32_e32 v75, 24, v77
	v_pk_add_f32 v[66:67], v[66:67], s[16:17] op_sel_hi:[1,0]
	v_lshlrev_b32_e32 v69, 8, v69
	v_lshlrev_b32_e32 v74, 16, v74
	v_or_b32_e32 v73, v73, v75
	v_and_b32_e32 v69, 0xff00, v69
	v_and_b32_e32 v74, 0xff0000, v74
	v_lshlrev_b32_e32 v76, 24, v76
	v_or_b32_sdwa v67, v73, v67 dst_sel:DWORD dst_unused:UNUSED_PAD src0_sel:DWORD src1_sel:BYTE_0
	v_mul_f32_e32 v73, 0x44800000, v43
	v_or_b32_e32 v74, v74, v76
	v_or_b32_e32 v67, v67, v69
	v_mul_f32_e32 v69, 0x44800000, v39
	v_mul_f32_e32 v75, 0x44800000, v47
	v_med3_f32 v76, v73, s70, v72
	v_mul_f32_e32 v73, 0x44800000, v55
	v_mul_f32_e32 v77, 0x44800000, v59
	v_lshlrev_b32_e32 v68, 8, v68
	v_or_b32_sdwa v66, v74, v66 dst_sel:DWORD dst_unused:UNUSED_PAD src0_sel:DWORD src1_sel:BYTE_0
	v_med3_f32 v74, v69, s70, v72
	v_med3_f32 v78, v75, s70, v72
	v_mul_f32_e32 v79, 0x44800000, v63
	v_med3_f32 v75, v73, s70, v72
	v_med3_f32 v77, v77, s70, v72
	v_and_b32_e32 v68, 0xff00, v68
	v_med3_f32 v79, v79, s70, v72
	v_pk_add_f32 v[74:75], v[74:75], s[16:17] op_sel_hi:[1,0]
	v_pk_add_f32 v[76:77], v[76:77], s[16:17] op_sel_hi:[1,0]
	v_or_b32_e32 v66, v66, v68
	v_mul_f32_e32 v68, 0x44800000, v35
	v_mul_f32_e32 v69, 0x44800000, v51
	v_pk_add_f32 v[78:79], v[78:79], s[16:17] op_sel_hi:[1,0]
	v_lshlrev_b32_e32 v73, 8, v75
	v_lshlrev_b32_e32 v75, 16, v77
	v_lshlrev_b32_e32 v76, 16, v76
	v_med3_f32 v68, v68, s70, v72
	v_med3_f32 v69, v69, s70, v72
	v_and_b32_e32 v75, 0xff0000, v75
	v_and_b32_e32 v76, 0xff0000, v76
	v_lshlrev_b32_e32 v77, 24, v79
	v_lshlrev_b32_e32 v78, 24, v78
	v_pk_add_f32 v[68:69], v[68:69], s[16:17] op_sel_hi:[1,0]
	v_lshlrev_b32_e32 v74, 8, v74
	v_or_b32_e32 v75, v75, v77
	v_or_b32_e32 v76, v76, v78
	v_and_b32_e32 v73, 0xff00, v73
	v_and_b32_e32 v74, 0xff00, v74
	v_or_b32_sdwa v69, v75, v69 dst_sel:DWORD dst_unused:UNUSED_PAD src0_sel:DWORD src1_sel:BYTE_0
	v_or_b32_sdwa v68, v76, v68 dst_sel:DWORD dst_unused:UNUSED_PAD src0_sel:DWORD src1_sel:BYTE_0
	v_or_b32_e32 v69, v69, v73
	v_or_b32_e32 v68, v68, v74
	v_mul_f32_e32 v73, 0x44800000, v16
	ds_write_b128 v70, v[66:69] offset:528
	v_mul_f32_e32 v69, 0x44800000, v12
	v_med3_f32 v76, v73, s70, v72
	v_mul_f32_e32 v73, 0x44800000, v28
	v_med3_f32 v74, v69, s70, v72
	v_mul_f32_e32 v77, 0x44800000, v32
	v_med3_f32 v75, v73, s70, v72
	v_mul_f32_e32 v67, 0x44800000, v8
	v_mul_f32_e32 v69, 0x44800000, v24
	v_med3_f32 v77, v77, s70, v72
	v_pk_add_f32 v[74:75], v[74:75], s[16:17] op_sel_hi:[1,0]
	v_mul_f32_e32 v66, 0x44800000, v4
	v_med3_f32 v68, v67, s70, v72
	v_mul_f32_e32 v67, 0x44800000, v20
	v_med3_f32 v69, v69, s70, v72
	v_pk_add_f32 v[76:77], v[76:77], s[16:17] op_sel_hi:[1,0]
	v_lshlrev_b32_e32 v73, 16, v75
	v_med3_f32 v66, v66, s70, v72
	v_med3_f32 v67, v67, s70, v72
	v_pk_add_f32 v[68:69], v[68:69], s[16:17] op_sel_hi:[1,0]
	v_and_b32_e32 v73, 0xff0000, v73
	v_lshlrev_b32_e32 v75, 24, v77
	v_pk_add_f32 v[66:67], v[66:67], s[16:17] op_sel_hi:[1,0]
	v_lshlrev_b32_e32 v69, 8, v69
	v_lshlrev_b32_e32 v74, 16, v74
	v_or_b32_e32 v73, v73, v75
	v_and_b32_e32 v69, 0xff00, v69
	v_and_b32_e32 v74, 0xff0000, v74
	v_lshlrev_b32_e32 v76, 24, v76
	v_or_b32_sdwa v67, v73, v67 dst_sel:DWORD dst_unused:UNUSED_PAD src0_sel:DWORD src1_sel:BYTE_0
	v_mul_f32_e32 v73, 0x44800000, v44
	v_or_b32_e32 v74, v74, v76
	v_or_b32_e32 v67, v67, v69
	v_mul_f32_e32 v69, 0x44800000, v40
	v_mul_f32_e32 v75, 0x44800000, v48
	v_med3_f32 v76, v73, s70, v72
	v_mul_f32_e32 v73, 0x44800000, v56
	v_mul_f32_e32 v77, 0x44800000, v60
	v_lshlrev_b32_e32 v68, 8, v68
	v_or_b32_sdwa v66, v74, v66 dst_sel:DWORD dst_unused:UNUSED_PAD src0_sel:DWORD src1_sel:BYTE_0
	v_med3_f32 v74, v69, s70, v72
	v_med3_f32 v78, v75, s70, v72
	v_mul_f32_e32 v79, 0x44800000, v64
	v_med3_f32 v75, v73, s70, v72
	v_med3_f32 v77, v77, s70, v72
	v_and_b32_e32 v68, 0xff00, v68
	v_med3_f32 v79, v79, s70, v72
	v_pk_add_f32 v[74:75], v[74:75], s[16:17] op_sel_hi:[1,0]
	v_pk_add_f32 v[76:77], v[76:77], s[16:17] op_sel_hi:[1,0]
	v_or_b32_e32 v66, v66, v68
	v_mul_f32_e32 v68, 0x44800000, v36
	v_mul_f32_e32 v69, 0x44800000, v52
	v_pk_add_f32 v[78:79], v[78:79], s[16:17] op_sel_hi:[1,0]
	v_lshlrev_b32_e32 v73, 8, v75
	v_lshlrev_b32_e32 v75, 16, v77
	v_lshlrev_b32_e32 v76, 16, v76
	v_med3_f32 v68, v68, s70, v72
	v_med3_f32 v69, v69, s70, v72
	v_and_b32_e32 v75, 0xff0000, v75
	v_and_b32_e32 v76, 0xff0000, v76
	v_lshlrev_b32_e32 v77, 24, v79
	v_lshlrev_b32_e32 v78, 24, v78
	v_pk_add_f32 v[68:69], v[68:69], s[16:17] op_sel_hi:[1,0]
	v_lshlrev_b32_e32 v74, 8, v74
	v_or_b32_e32 v75, v75, v77
	v_or_b32_e32 v76, v76, v78
	v_and_b32_e32 v73, 0xff00, v73
	v_and_b32_e32 v74, 0xff00, v74
	v_or_b32_sdwa v69, v75, v69 dst_sel:DWORD dst_unused:UNUSED_PAD src0_sel:DWORD src1_sel:BYTE_0
	v_or_b32_sdwa v68, v76, v68 dst_sel:DWORD dst_unused:UNUSED_PAD src0_sel:DWORD src1_sel:BYTE_0
	v_or_b32_e32 v69, v69, v73
	v_or_b32_e32 v68, v68, v74
	v_mul_f32_e32 v73, 0x44800000, v17
	ds_write_b128 v70, v[66:69] offset:1056
	v_mul_f32_e32 v69, 0x44800000, v13
	v_med3_f32 v76, v73, s70, v72
	v_mul_f32_e32 v73, 0x44800000, v29
	v_med3_f32 v74, v69, s70, v72
	v_mul_f32_e32 v77, 0x44800000, v33
	v_med3_f32 v75, v73, s70, v72
	v_mul_f32_e32 v67, 0x44800000, v9
	v_mul_f32_e32 v69, 0x44800000, v25
	v_med3_f32 v77, v77, s70, v72
	v_pk_add_f32 v[74:75], v[74:75], s[16:17] op_sel_hi:[1,0]
	v_mul_f32_e32 v66, 0x44800000, v5
	v_med3_f32 v68, v67, s70, v72
	v_mul_f32_e32 v67, 0x44800000, v21
	v_med3_f32 v69, v69, s70, v72
	v_pk_add_f32 v[76:77], v[76:77], s[16:17] op_sel_hi:[1,0]
	v_lshlrev_b32_e32 v73, 16, v75
	v_med3_f32 v66, v66, s70, v72
	v_med3_f32 v67, v67, s70, v72
	v_pk_add_f32 v[68:69], v[68:69], s[16:17] op_sel_hi:[1,0]
	v_and_b32_e32 v73, 0xff0000, v73
	v_lshlrev_b32_e32 v75, 24, v77
	v_pk_add_f32 v[66:67], v[66:67], s[16:17] op_sel_hi:[1,0]
	v_lshlrev_b32_e32 v69, 8, v69
	v_lshlrev_b32_e32 v74, 16, v74
	v_or_b32_e32 v73, v73, v75
	v_and_b32_e32 v69, 0xff00, v69
	v_and_b32_e32 v74, 0xff0000, v74
	v_lshlrev_b32_e32 v76, 24, v76
	v_or_b32_sdwa v67, v73, v67 dst_sel:DWORD dst_unused:UNUSED_PAD src0_sel:DWORD src1_sel:BYTE_0
	v_mul_f32_e32 v73, 0x44800000, v45
	v_or_b32_e32 v74, v74, v76
	v_or_b32_e32 v67, v67, v69
	v_mul_f32_e32 v69, 0x44800000, v41
	v_mul_f32_e32 v75, 0x44800000, v49
	v_med3_f32 v76, v73, s70, v72
	v_mul_f32_e32 v73, 0x44800000, v57
	v_mul_f32_e32 v77, 0x44800000, v61
	v_lshlrev_b32_e32 v68, 8, v68
	v_or_b32_sdwa v66, v74, v66 dst_sel:DWORD dst_unused:UNUSED_PAD src0_sel:DWORD src1_sel:BYTE_0
	v_med3_f32 v74, v69, s70, v72
	v_med3_f32 v78, v75, s70, v72
	v_mul_f32_e32 v79, 0x44800000, v65
	v_med3_f32 v75, v73, s70, v72
	v_med3_f32 v77, v77, s70, v72
	v_and_b32_e32 v68, 0xff00, v68
	v_med3_f32 v79, v79, s70, v72
	v_pk_add_f32 v[74:75], v[74:75], s[16:17] op_sel_hi:[1,0]
	v_pk_add_f32 v[76:77], v[76:77], s[16:17] op_sel_hi:[1,0]
	v_or_b32_e32 v66, v66, v68
	v_mul_f32_e32 v68, 0x44800000, v37
	v_mul_f32_e32 v69, 0x44800000, v53
	v_pk_add_f32 v[78:79], v[78:79], s[16:17] op_sel_hi:[1,0]
	v_lshlrev_b32_e32 v73, 8, v75
	v_lshlrev_b32_e32 v75, 16, v77
	v_lshlrev_b32_e32 v76, 16, v76
	v_med3_f32 v68, v68, s70, v72
	v_med3_f32 v69, v69, s70, v72
	v_and_b32_e32 v75, 0xff0000, v75
	v_and_b32_e32 v76, 0xff0000, v76
	v_lshlrev_b32_e32 v77, 24, v79
	v_lshlrev_b32_e32 v78, 24, v78
	v_pk_add_f32 v[68:69], v[68:69], s[16:17] op_sel_hi:[1,0]
	v_lshlrev_b32_e32 v74, 8, v74
	v_or_b32_e32 v75, v75, v77
	v_or_b32_e32 v76, v76, v78
	v_and_b32_e32 v73, 0xff00, v73
	v_and_b32_e32 v74, 0xff00, v74
	v_or_b32_sdwa v69, v75, v69 dst_sel:DWORD dst_unused:UNUSED_PAD src0_sel:DWORD src1_sel:BYTE_0
	v_or_b32_sdwa v68, v76, v68 dst_sel:DWORD dst_unused:UNUSED_PAD src0_sel:DWORD src1_sel:BYTE_0
	v_or_b32_e32 v69, v69, v73
	v_or_b32_e32 v68, v68, v74
	ds_write_b128 v70, v[66:69] offset:1584
	s_mov_b64 s[28:29], 0

.LBB0_2358:
	s_cmp_ge_u32 s17, s33
	v_mov_b32_e32 v66, 0x26a0
	s_cbranch_scc1 .LBB0_2362
	s_mov_b64 s[30:31], exec
	v_mbcnt_lo_u32_b32 v66, s30, 0
	v_mbcnt_hi_u32_b32 v66, s31, v66
	v_cmp_eq_u32_e32 vcc, 0, v66
	s_and_saveexec_b64 s[28:29], vcc
	s_cbranch_execz .LBB0_2361
	s_bcnt1_i32_b64 s18, s[30:31]
	v_mov_b32_e32 v67, s18
	v_mov_b32_e32 v67, v253

.LBB0_2641:
	s_and_saveexec_b64 s[2:3], s[0:1]
	s_cbranch_execz .Lec_5_rest
	v_mov_b32_e32 v253, 1
	global_atomic_add v253, v71, v253, s[94:95] offset:1536 sc0
.Lec_5_rest:
	s_or_b64 exec, exec, s[2:3]
	s_mov_b32 s21, s76
	s_mov_b32 s23, s54
	s_mov_b32 s20, s77
	s_mov_b32 s11, s25
	s_mov_b32 s22, s71
	s_mov_b32 s10, s24
	s_mov_b64 s[26:27], s[52:53]
	s_mov_b64 s[30:31], -1
	s_mov_b64 s[2:3], 0
	s_cmp_lt_i32 s76, 2
	s_mov_b64 s[28:29], 0
	s_cbranch_scc1 .LBB0_2648
	s_cmp_eq_u32 s21, 2
	s_mov_b64 s[28:29], -1
	s_cbranch_scc0 .LBB0_2644
	s_waitcnt vmcnt(12)
	v_mul_f32_e32 v70, 0x44800000, v14
	v_mul_f32_e32 v69, 0x44800000, v10
	v_med3_f32 v76, v70, s69, v72
	s_waitcnt vmcnt(9)
	v_mul_f32_e32 v70, 0x44800000, v26
	v_med3_f32 v74, v69, s69, v72
	s_waitcnt vmcnt(8)
	v_mul_f32_e32 v73, 0x44800000, v30
	v_med3_f32 v75, v70, s69, v72
	v_mul_f32_e32 v67, 0x44800000, v6
	v_mul_f32_e32 v69, 0x44800000, v22
	v_med3_f32 v77, v73, s69, v72
	v_pk_add_f32 v[74:75], v[74:75], s[16:17] op_sel_hi:[1,0]
	v_mul_f32_e32 v66, 0x44800000, v2
	v_med3_f32 v68, v67, s69, v72
	v_mul_f32_e32 v67, 0x44800000, v18
	v_med3_f32 v69, v69, s69, v72
	v_pk_add_f32 v[76:77], v[76:77], s[16:17] op_sel_hi:[1,0]
	v_lshlrev_b32_e32 v70, 16, v75
	v_lshlrev_b32_e32 v73, 16, v74
	v_med3_f32 v66, v66, s69, v72
	v_med3_f32 v67, v67, s69, v72
	v_pk_add_f32 v[68:69], v[68:69], s[16:17] op_sel_hi:[1,0]
	v_and_b32_e32 v70, 0xff0000, v70
	v_and_b32_e32 v73, 0xff0000, v73
	v_lshlrev_b32_e32 v74, 24, v77
	v_lshlrev_b32_e32 v75, 24, v76
	v_pk_add_f32 v[66:67], v[66:67], s[16:17] op_sel_hi:[1,0]
	v_lshlrev_b32_e32 v69, 8, v69
	v_or_b32_e32 v70, v70, v74
	v_or_b32_e32 v73, v73, v75
	v_and_b32_e32 v69, 0xff00, v69
	v_or_b32_sdwa v67, v70, v67 dst_sel:DWORD dst_unused:UNUSED_PAD src0_sel:DWORD src1_sel:BYTE_0
	v_or_b32_sdwa v66, v73, v66 dst_sel:DWORD dst_unused:UNUSED_PAD src0_sel:DWORD src1_sel:BYTE_0
	s_waitcnt vmcnt(5)
	v_mul_f32_e32 v70, 0x44800000, v42
	s_waitcnt vmcnt(4)
	v_mul_f32_e32 v73, 0x44800000, v46
	v_or_b32_e32 v67, v67, v69
	v_mul_f32_e32 v69, 0x44800000, v38
	v_med3_f32 v76, v70, s69, v72
	v_med3_f32 v78, v73, s69, v72
	s_waitcnt vmcnt(2)
	v_mul_f32_e32 v70, 0x44800000, v54
	s_waitcnt vmcnt(1)
	v_mul_f32_e32 v73, 0x44800000, v58
	v_lshlrev_b32_e32 v68, 8, v68
	v_med3_f32 v74, v69, s69, v72
	s_waitcnt vmcnt(0)
	v_mul_f32_e32 v79, 0x44800000, v62
	v_med3_f32 v75, v70, s69, v72
	v_med3_f32 v77, v73, s69, v72
	v_and_b32_e32 v68, 0xff00, v68
	v_med3_f32 v79, v79, s69, v72
	v_pk_add_f32 v[74:75], v[74:75], s[16:17] op_sel_hi:[1,0]
	v_pk_add_f32 v[76:77], v[76:77], s[16:17] op_sel_hi:[1,0]
	v_or_b32_e32 v66, v66, v68
	v_mul_f32_e32 v68, 0x44800000, v34
	v_mul_f32_e32 v69, 0x44800000, v50
	v_pk_add_f32 v[78:79], v[78:79], s[16:17] op_sel_hi:[1,0]
	v_lshlrev_b32_e32 v70, 8, v75
	v_lshlrev_b32_e32 v73, 8, v74
	v_lshlrev_b32_e32 v74, 16, v77
	v_lshlrev_b32_e32 v75, 16, v76
	v_med3_f32 v68, v68, s69, v72
	v_med3_f32 v69, v69, s69, v72
	v_and_b32_e32 v74, 0xff0000, v74
	v_and_b32_e32 v75, 0xff0000, v75
	v_lshlrev_b32_e32 v76, 24, v79
	v_lshlrev_b32_e32 v77, 24, v78
	v_pk_add_f32 v[68:69], v[68:69], s[16:17] op_sel_hi:[1,0]
	v_or_b32_e32 v74, v74, v76
	v_or_b32_e32 v75, v75, v77
	v_and_b32_e32 v70, 0xff00, v70
	v_and_b32_e32 v73, 0xff00, v73
	v_or_b32_sdwa v69, v74, v69 dst_sel:DWORD dst_unused:UNUSED_PAD src0_sel:DWORD src1_sel:BYTE_0
	v_or_b32_sdwa v68, v75, v68 dst_sel:DWORD dst_unused:UNUSED_PAD src0_sel:DWORD src1_sel:BYTE_0
	v_or_b32_e32 v69, v69, v70
	v_or_b32_e32 v68, v68, v73
	v_add_u32_e32 v70, v199, v198
	v_mul_f32_e32 v73, 0x44800000, v15
	ds_write_b128 v70, v[66:69]
	v_mul_f32_e32 v69, 0x44800000, v11
	v_med3_f32 v76, v73, s69, v72
	v_mul_f32_e32 v73, 0x44800000, v27
	v_med3_f32 v74, v69, s69, v72
	v_mul_f32_e32 v77, 0x44800000, v31
	v_med3_f32 v75, v73, s69, v72
	v_mul_f32_e32 v67, 0x44800000, v7
	v_mul_f32_e32 v69, 0x44800000, v23
	v_med3_f32 v77, v77, s69, v72
	v_pk_add_f32 v[74:75], v[74:75], s[16:17] op_sel_hi:[1,0]
	v_mul_f32_e32 v66, 0x44800000, v3
	v_med3_f32 v68, v67, s69, v72
	v_mul_f32_e32 v67, 0x44800000, v19
	v_med3_f32 v69, v69, s69, v72
	v_pk_add_f32 v[76:77], v[76:77], s[16:17] op_sel_hi:[1,0]
	v_lshlrev_b32_e32 v73, 16, v75
	v_med3_f32 v66, v66, s69, v72
	v_med3_f32 v67, v67, s69, v72
	v_pk_add_f32 v[68:69], v[68:69], s[16:17] op_sel_hi:[1,0]
	v_and_b32_e32 v73, 0xff0000, v73
	v_lshlrev_b32_e32 v75, 24, v77
	v_pk_add_f32 v[66:67], v[66:67], s[16:17] op_sel_hi:[1,0]
	v_lshlrev_b32_e32 v69, 8, v69
	v_lshlrev_b32_e32 v74, 16, v74
	v_or_b32_e32 v73, v73, v75
	v_and_b32_e32 v69, 0xff00, v69
	v_and_b32_e32 v74, 0xff0000, v74
	v_lshlrev_b32_e32 v76, 24, v76
	v_or_b32_sdwa v67, v73, v67 dst_sel:DWORD dst_unused:UNUSED_PAD src0_sel:DWORD src1_sel:BYTE_0
	v_mul_f32_e32 v73, 0x44800000, v43
	v_or_b32_e32 v74, v74, v76
	v_or_b32_e32 v67, v67, v69
	v_mul_f32_e32 v69, 0x44800000, v39
	v_mul_f32_e32 v75, 0x44800000, v47
	v_med3_f32 v76, v73, s69, v72
	v_mul_f32_e32 v73, 0x44800000, v55
	v_mul_f32_e32 v77, 0x44800000, v59
	v_lshlrev_b32_e32 v68, 8, v68
	v_or_b32_sdwa v66, v74, v66 dst_sel:DWORD dst_unused:UNUSED_PAD src0_sel:DWORD src1_sel:BYTE_0
	v_med3_f32 v74, v69, s69, v72
	v_med3_f32 v78, v75, s69, v72
	v_mul_f32_e32 v79, 0x44800000, v63
	v_med3_f32 v75, v73, s69, v72
	v_med3_f32 v77, v77, s69, v72
	v_and_b32_e32 v68, 0xff00, v68
	v_med3_f32 v79, v79, s69, v72
	v_pk_add_f32 v[74:75], v[74:75], s[16:17] op_sel_hi:[1,0]
	v_pk_add_f32 v[76:77], v[76:77], s[16:17] op_sel_hi:[1,0]
	v_or_b32_e32 v66, v66, v68
	v_mul_f32_e32 v68, 0x44800000, v35
	v_mul_f32_e32 v69, 0x44800000, v51
	v_pk_add_f32 v[78:79], v[78:79], s[16:17] op_sel_hi:[1,0]
	v_lshlrev_b32_e32 v73, 8, v75
	v_lshlrev_b32_e32 v75, 16, v77
	v_lshlrev_b32_e32 v76, 16, v76
	v_med3_f32 v68, v68, s69, v72
	v_med3_f32 v69, v69, s69, v72
	v_and_b32_e32 v75, 0xff0000, v75
	v_and_b32_e32 v76, 0xff0000, v76
	v_lshlrev_b32_e32 v77, 24, v79
	v_lshlrev_b32_e32 v78, 24, v78
	v_pk_add_f32 v[68:69], v[68:69], s[16:17] op_sel_hi:[1,0]
	v_lshlrev_b32_e32 v74, 8, v74
	v_or_b32_e32 v75, v75, v77
	v_or_b32_e32 v76, v76, v78
	v_and_b32_e32 v73, 0xff00, v73
	v_and_b32_e32 v74, 0xff00, v74
	v_or_b32_sdwa v69, v75, v69 dst_sel:DWORD dst_unused:UNUSED_PAD src0_sel:DWORD src1_sel:BYTE_0
	v_or_b32_sdwa v68, v76, v68 dst_sel:DWORD dst_unused:UNUSED_PAD src0_sel:DWORD src1_sel:BYTE_0
	v_or_b32_e32 v69, v69, v73
	v_or_b32_e32 v68, v68, v74
	v_mul_f32_e32 v73, 0x44800000, v16
	ds_write_b128 v70, v[66:69] offset:528
	v_mul_f32_e32 v69, 0x44800000, v12
	v_med3_f32 v76, v73, s69, v72
	v_mul_f32_e32 v73, 0x44800000, v28
	v_med3_f32 v74, v69, s69, v72
	v_mul_f32_e32 v77, 0x44800000, v32
	v_med3_f32 v75, v73, s69, v72
	v_mul_f32_e32 v67, 0x44800000, v8
	v_mul_f32_e32 v69, 0x44800000, v24
	v_med3_f32 v77, v77, s69, v72
	v_pk_add_f32 v[74:75], v[74:75], s[16:17] op_sel_hi:[1,0]
	v_mul_f32_e32 v66, 0x44800000, v4
	v_med3_f32 v68, v67, s69, v72
	v_mul_f32_e32 v67, 0x44800000, v20
	v_med3_f32 v69, v69, s69, v72
	v_pk_add_f32 v[76:77], v[76:77], s[16:17] op_sel_hi:[1,0]
	v_lshlrev_b32_e32 v73, 16, v75
	v_med3_f32 v66, v66, s69, v72
	v_med3_f32 v67, v67, s69, v72
	v_pk_add_f32 v[68:69], v[68:69], s[16:17] op_sel_hi:[1,0]
	v_and_b32_e32 v73, 0xff0000, v73
	v_lshlrev_b32_e32 v75, 24, v77
	v_pk_add_f32 v[66:67], v[66:67], s[16:17] op_sel_hi:[1,0]
	v_lshlrev_b32_e32 v69, 8, v69
	v_lshlrev_b32_e32 v74, 16, v74
	v_or_b32_e32 v73, v73, v75
	v_and_b32_e32 v69, 0xff00, v69
	v_and_b32_e32 v74, 0xff0000, v74
	v_lshlrev_b32_e32 v76, 24, v76
	v_or_b32_sdwa v67, v73, v67 dst_sel:DWORD dst_unused:UNUSED_PAD src0_sel:DWORD src1_sel:BYTE_0
	v_mul_f32_e32 v73, 0x44800000, v44
	v_or_b32_e32 v74, v74, v76
	v_or_b32_e32 v67, v67, v69
	v_mul_f32_e32 v69, 0x44800000, v40
	v_mul_f32_e32 v75, 0x44800000, v48
	v_med3_f32 v76, v73, s69, v72
	v_mul_f32_e32 v73, 0x44800000, v56
	v_mul_f32_e32 v77, 0x44800000, v60
	v_lshlrev_b32_e32 v68, 8, v68
	v_or_b32_sdwa v66, v74, v66 dst_sel:DWORD dst_unused:UNUSED_PAD src0_sel:DWORD src1_sel:BYTE_0
	v_med3_f32 v74, v69, s69, v72
	v_med3_f32 v78, v75, s69, v72
	v_mul_f32_e32 v79, 0x44800000, v64
	v_med3_f32 v75, v73, s69, v72
	v_med3_f32 v77, v77, s69, v72
	v_and_b32_e32 v68, 0xff00, v68
	v_med3_f32 v79, v79, s69, v72
	v_pk_add_f32 v[74:75], v[74:75], s[16:17] op_sel_hi:[1,0]
	v_pk_add_f32 v[76:77], v[76:77], s[16:17] op_sel_hi:[1,0]
	v_or_b32_e32 v66, v66, v68
	v_mul_f32_e32 v68, 0x44800000, v36
	v_mul_f32_e32 v69, 0x44800000, v52
	v_pk_add_f32 v[78:79], v[78:79], s[16:17] op_sel_hi:[1,0]
	v_lshlrev_b32_e32 v73, 8, v75
	v_lshlrev_b32_e32 v75, 16, v77
	v_lshlrev_b32_e32 v76, 16, v76
	v_med3_f32 v68, v68, s69, v72
	v_med3_f32 v69, v69, s69, v72
	v_and_b32_e32 v75, 0xff0000, v75
	v_and_b32_e32 v76, 0xff0000, v76
	v_lshlrev_b32_e32 v77, 24, v79
	v_lshlrev_b32_e32 v78, 24, v78
	v_pk_add_f32 v[68:69], v[68:69], s[16:17] op_sel_hi:[1,0]
	v_lshlrev_b32_e32 v74, 8, v74
	v_or_b32_e32 v75, v75, v77
	v_or_b32_e32 v76, v76, v78
	v_and_b32_e32 v73, 0xff00, v73
	v_and_b32_e32 v74, 0xff00, v74
	v_or_b32_sdwa v69, v75, v69 dst_sel:DWORD dst_unused:UNUSED_PAD src0_sel:DWORD src1_sel:BYTE_0
	v_or_b32_sdwa v68, v76, v68 dst_sel:DWORD dst_unused:UNUSED_PAD src0_sel:DWORD src1_sel:BYTE_0
	v_or_b32_e32 v69, v69, v73
	v_or_b32_e32 v68, v68, v74
	v_mul_f32_e32 v73, 0x44800000, v17
	ds_write_b128 v70, v[66:69] offset:1056
	v_mul_f32_e32 v69, 0x44800000, v13
	v_med3_f32 v76, v73, s69, v72
	v_mul_f32_e32 v73, 0x44800000, v29
	v_med3_f32 v74, v69, s69, v72
	v_mul_f32_e32 v77, 0x44800000, v33
	v_med3_f32 v75, v73, s69, v72
	v_mul_f32_e32 v67, 0x44800000, v9
	v_mul_f32_e32 v69, 0x44800000, v25
	v_med3_f32 v77, v77, s69, v72
	v_pk_add_f32 v[74:75], v[74:75], s[16:17] op_sel_hi:[1,0]
	v_mul_f32_e32 v66, 0x44800000, v5
	v_med3_f32 v68, v67, s69, v72
	v_mul_f32_e32 v67, 0x44800000, v21
	v_med3_f32 v69, v69, s69, v72
	v_pk_add_f32 v[76:77], v[76:77], s[16:17] op_sel_hi:[1,0]
	v_lshlrev_b32_e32 v73, 16, v75
	v_med3_f32 v66, v66, s69, v72
	v_med3_f32 v67, v67, s69, v72
	v_pk_add_f32 v[68:69], v[68:69], s[16:17] op_sel_hi:[1,0]
	v_and_b32_e32 v73, 0xff0000, v73
	v_lshlrev_b32_e32 v75, 24, v77
	v_pk_add_f32 v[66:67], v[66:67], s[16:17] op_sel_hi:[1,0]
	v_lshlrev_b32_e32 v69, 8, v69
	v_lshlrev_b32_e32 v74, 16, v74
	v_or_b32_e32 v73, v73, v75
	v_and_b32_e32 v69, 0xff00, v69
	v_and_b32_e32 v74, 0xff0000, v74
	v_lshlrev_b32_e32 v76, 24, v76
	v_or_b32_sdwa v67, v73, v67 dst_sel:DWORD dst_unused:UNUSED_PAD src0_sel:DWORD src1_sel:BYTE_0
	v_mul_f32_e32 v73, 0x44800000, v45
	v_or_b32_e32 v74, v74, v76
	v_or_b32_e32 v67, v67, v69
	v_mul_f32_e32 v69, 0x44800000, v41
	v_mul_f32_e32 v75, 0x44800000, v49
	v_med3_f32 v76, v73, s69, v72
	v_mul_f32_e32 v73, 0x44800000, v57
	v_mul_f32_e32 v77, 0x44800000, v61
	v_lshlrev_b32_e32 v68, 8, v68
	v_or_b32_sdwa v66, v74, v66 dst_sel:DWORD dst_unused:UNUSED_PAD src0_sel:DWORD src1_sel:BYTE_0
	v_med3_f32 v74, v69, s69, v72
	v_med3_f32 v78, v75, s69, v72
	v_mul_f32_e32 v79, 0x44800000, v65
	v_med3_f32 v75, v73, s69, v72
	v_med3_f32 v77, v77, s69, v72
	v_and_b32_e32 v68, 0xff00, v68
	v_med3_f32 v79, v79, s69, v72
	v_pk_add_f32 v[74:75], v[74:75], s[16:17] op_sel_hi:[1,0]
	v_pk_add_f32 v[76:77], v[76:77], s[16:17] op_sel_hi:[1,0]
	v_or_b32_e32 v66, v66, v68
	v_mul_f32_e32 v68, 0x44800000, v37
	v_mul_f32_e32 v69, 0x44800000, v53
	v_pk_add_f32 v[78:79], v[78:79], s[16:17] op_sel_hi:[1,0]
	v_lshlrev_b32_e32 v73, 8, v75
	v_lshlrev_b32_e32 v75, 16, v77
	v_lshlrev_b32_e32 v76, 16, v76
	v_med3_f32 v68, v68, s69, v72
	v_med3_f32 v69, v69, s69, v72
	v_and_b32_e32 v75, 0xff0000, v75
	v_and_b32_e32 v76, 0xff0000, v76
	v_lshlrev_b32_e32 v77, 24, v79
	v_lshlrev_b32_e32 v78, 24, v78
	v_pk_add_f32 v[68:69], v[68:69], s[16:17] op_sel_hi:[1,0]
	v_lshlrev_b32_e32 v74, 8, v74
	v_or_b32_e32 v75, v75, v77
	v_or_b32_e32 v76, v76, v78
	v_and_b32_e32 v73, 0xff00, v73
	v_and_b32_e32 v74, 0xff00, v74
	v_or_b32_sdwa v69, v75, v69 dst_sel:DWORD dst_unused:UNUSED_PAD src0_sel:DWORD src1_sel:BYTE_0
	v_or_b32_sdwa v68, v76, v68 dst_sel:DWORD dst_unused:UNUSED_PAD src0_sel:DWORD src1_sel:BYTE_0
	v_or_b32_e32 v69, v69, v73
	v_or_b32_e32 v68, v68, v74
	ds_write_b128 v70, v[66:69] offset:1584
	s_mov_b64 s[28:29], 0

.LBB0_2652:
	s_cmp_eq_u32 s68, 0
	s_cbranch_scc1 .LBB0_2656
	s_mov_b64 s[30:31], exec
	v_mbcnt_lo_u32_b32 v66, s30, 0
	v_mbcnt_hi_u32_b32 v66, s31, v66
	v_cmp_eq_u32_e32 vcc, 0, v66
	s_and_saveexec_b64 s[28:29], vcc
	s_cbranch_execz .LBB0_2655
	s_bcnt1_i32_b64 s18, s[30:31]
	v_mov_b32_e32 v67, s18
	v_mov_b32_e32 v67, v253

.LBB0_3185:
	s_and_saveexec_b64 s[2:3], s[0:1]
	s_cbranch_execz .Lec_6_rest
	v_mov_b32_e32 v253, 1
	global_atomic_add v253, v71, v253, s[94:95] offset:2048 sc0
.Lec_6_rest:
	s_or_b64 exec, exec, s[2:3]
	s_mov_b32 s17, s68
	s_mov_b32 s64, s22
	s_mov_b32 s16, s69
	s_mov_b32 s25, s66
	s_mov_b32 s63, s67
	s_mov_b32 s24, s65
	s_mov_b64 s[18:19], s[20:21]
	s_mov_b64 s[22:23], -1
	s_mov_b64 s[2:3], 0
	s_cmp_lt_i32 s68, 2
	s_mov_b64 s[20:21], 0
	s_cbranch_scc1 .LBB0_3192
	s_cmp_eq_u32 s17, 2
	s_mov_b64 s[20:21], -1
	s_cbranch_scc0 .LBB0_3188
	s_waitcnt vmcnt(12)
	v_mul_f32_e32 v77, 0x44800000, v14
	v_mul_f32_e32 v69, 0x44800000, v10
	v_med3_f32 v90, v77, s60, v86
	s_waitcnt vmcnt(9)
	v_mul_f32_e32 v77, 0x44800000, v26
	v_med3_f32 v76, v69, s60, v86
	s_waitcnt vmcnt(8)
	v_mul_f32_e32 v89, 0x44800000, v30
	v_med3_f32 v77, v77, s60, v86
	v_mul_f32_e32 v67, 0x44800000, v6
	v_med3_f32 v91, v89, s60, v86
	v_pk_add_f32 v[76:77], v[76:77], s[14:15] op_sel_hi:[1,0]
	v_mul_f32_e32 v66, 0x44800000, v2
	v_med3_f32 v68, v67, s60, v86
	v_mul_f32_e32 v67, 0x44800000, v18
	v_mul_f32_e32 v69, 0x44800000, v22
	v_pk_add_f32 v[90:91], v[90:91], s[14:15] op_sel_hi:[1,0]
	v_lshlrev_b32_e32 v77, 16, v77
	v_med3_f32 v66, v66, s60, v86
	v_med3_f32 v67, v67, s60, v86
	v_med3_f32 v69, v69, s60, v86
	v_and_b32_e32 v77, 0xff0000, v77
	v_lshlrev_b32_e32 v89, 24, v91
	v_pk_add_f32 v[66:67], v[66:67], s[14:15] op_sel_hi:[1,0]
	v_pk_add_f32 v[68:69], v[68:69], s[14:15] op_sel_hi:[1,0]
	v_lshlrev_b32_e32 v76, 16, v76
	v_or_b32_e32 v77, v77, v89
	s_waitcnt vmcnt(4)
	v_mul_f32_e32 v89, 0x44800000, v46
	v_lshlrev_b32_e32 v69, 8, v69
	v_and_b32_e32 v76, 0xff0000, v76
	v_lshlrev_b32_e32 v90, 24, v90
	v_or_b32_sdwa v67, v77, v67 dst_sel:DWORD dst_unused:UNUSED_PAD src0_sel:DWORD src1_sel:BYTE_0
	v_mul_f32_e32 v77, 0x44800000, v42
	v_med3_f32 v92, v89, s60, v86
	s_waitcnt vmcnt(1)
	v_mul_f32_e32 v89, 0x44800000, v58
	v_lshlrev_b32_e32 v68, 8, v68
	v_and_b32_e32 v69, 0xff00, v69
	v_or_b32_e32 v76, v76, v90
	v_med3_f32 v90, v77, s60, v86
	s_waitcnt vmcnt(0)
	v_mul_f32_e32 v93, 0x44800000, v62
	v_med3_f32 v91, v89, s60, v86
	v_and_b32_e32 v68, 0xff00, v68
	v_or_b32_sdwa v66, v76, v66 dst_sel:DWORD dst_unused:UNUSED_PAD src0_sel:DWORD src1_sel:BYTE_0
	v_or_b32_e32 v67, v67, v69
	v_mul_f32_e32 v69, 0x44800000, v38
	v_mul_f32_e32 v77, 0x44800000, v54
	v_med3_f32 v93, v93, s60, v86
	v_pk_add_f32 v[90:91], v[90:91], s[14:15] op_sel_hi:[1,0]
	v_or_b32_e32 v66, v66, v68
	v_mul_f32_e32 v68, 0x44800000, v34
	v_med3_f32 v76, v69, s60, v86
	v_mul_f32_e32 v69, 0x44800000, v50
	v_med3_f32 v77, v77, s60, v86
	v_pk_add_f32 v[92:93], v[92:93], s[14:15] op_sel_hi:[1,0]
	v_lshlrev_b32_e32 v89, 16, v91
	v_lshlrev_b32_e32 v90, 16, v90
	v_med3_f32 v68, v68, s60, v86
	v_med3_f32 v69, v69, s60, v86
	v_pk_add_f32 v[76:77], v[76:77], s[14:15] op_sel_hi:[1,0]
	v_and_b32_e32 v89, 0xff0000, v89
	v_and_b32_e32 v90, 0xff0000, v90
	v_lshlrev_b32_e32 v91, 24, v93
	v_lshlrev_b32_e32 v92, 24, v92
	v_pk_add_f32 v[68:69], v[68:69], s[14:15] op_sel_hi:[1,0]
	v_lshlrev_b32_e32 v77, 8, v77
	v_lshlrev_b32_e32 v76, 8, v76
	v_or_b32_e32 v89, v89, v91
	v_or_b32_e32 v90, v90, v92
	v_and_b32_e32 v77, 0xff00, v77
	v_and_b32_e32 v76, 0xff00, v76
	v_or_b32_sdwa v69, v89, v69 dst_sel:DWORD dst_unused:UNUSED_PAD src0_sel:DWORD src1_sel:BYTE_0
	v_or_b32_sdwa v68, v90, v68 dst_sel:DWORD dst_unused:UNUSED_PAD src0_sel:DWORD src1_sel:BYTE_0
	v_or_b32_e32 v69, v69, v77
	v_or_b32_e32 v68, v68, v76
	v_add_u32_e32 v89, v78, v75
	v_mul_f32_e32 v77, 0x44800000, v15
	ds_write_b128 v89, v[66:69]
	v_mul_f32_e32 v69, 0x44800000, v11
	v_med3_f32 v90, v77, s60, v86
	v_mul_f32_e32 v77, 0x44800000, v27
	v_med3_f32 v76, v69, s60, v86
	v_mul_f32_e32 v91, 0x44800000, v31
	v_med3_f32 v77, v77, s60, v86
	v_mul_f32_e32 v67, 0x44800000, v7
	v_med3_f32 v91, v91, s60, v86
	v_pk_add_f32 v[76:77], v[76:77], s[14:15] op_sel_hi:[1,0]
	v_mul_f32_e32 v66, 0x44800000, v3
	v_med3_f32 v68, v67, s60, v86
	v_mul_f32_e32 v67, 0x44800000, v19
	v_mul_f32_e32 v69, 0x44800000, v23
	v_pk_add_f32 v[90:91], v[90:91], s[14:15] op_sel_hi:[1,0]
	v_lshlrev_b32_e32 v77, 16, v77
	v_med3_f32 v66, v66, s60, v86
	v_med3_f32 v67, v67, s60, v86
	v_med3_f32 v69, v69, s60, v86
	v_and_b32_e32 v77, 0xff0000, v77
	v_lshlrev_b32_e32 v91, 24, v91
	v_pk_add_f32 v[66:67], v[66:67], s[14:15] op_sel_hi:[1,0]
	v_pk_add_f32 v[68:69], v[68:69], s[14:15] op_sel_hi:[1,0]
	v_lshlrev_b32_e32 v76, 16, v76
	v_or_b32_e32 v77, v77, v91
	v_mul_f32_e32 v91, 0x44800000, v47
	v_lshlrev_b32_e32 v69, 8, v69
	v_and_b32_e32 v76, 0xff0000, v76
	v_lshlrev_b32_e32 v90, 24, v90
	v_or_b32_sdwa v67, v77, v67 dst_sel:DWORD dst_unused:UNUSED_PAD src0_sel:DWORD src1_sel:BYTE_0
	v_mul_f32_e32 v77, 0x44800000, v43
	v_med3_f32 v92, v91, s60, v86
	v_mul_f32_e32 v91, 0x44800000, v59
	v_lshlrev_b32_e32 v68, 8, v68
	v_and_b32_e32 v69, 0xff00, v69
	v_or_b32_e32 v76, v76, v90
	v_med3_f32 v90, v77, s60, v86
	v_mul_f32_e32 v93, 0x44800000, v63
	v_med3_f32 v91, v91, s60, v86
	v_and_b32_e32 v68, 0xff00, v68
	v_or_b32_sdwa v66, v76, v66 dst_sel:DWORD dst_unused:UNUSED_PAD src0_sel:DWORD src1_sel:BYTE_0
	v_or_b32_e32 v67, v67, v69
	v_mul_f32_e32 v69, 0x44800000, v39
	v_mul_f32_e32 v77, 0x44800000, v55
	v_med3_f32 v93, v93, s60, v86
	v_pk_add_f32 v[90:91], v[90:91], s[14:15] op_sel_hi:[1,0]
	v_or_b32_e32 v66, v66, v68
	v_mul_f32_e32 v68, 0x44800000, v35
	v_med3_f32 v76, v69, s60, v86
	v_mul_f32_e32 v69, 0x44800000, v51
	v_med3_f32 v77, v77, s60, v86
	v_pk_add_f32 v[92:93], v[92:93], s[14:15] op_sel_hi:[1,0]
	v_lshlrev_b32_e32 v91, 16, v91
	v_lshlrev_b32_e32 v90, 16, v90
	v_med3_f32 v68, v68, s60, v86
	v_med3_f32 v69, v69, s60, v86
	v_pk_add_f32 v[76:77], v[76:77], s[14:15] op_sel_hi:[1,0]
	v_and_b32_e32 v91, 0xff0000, v91
	v_and_b32_e32 v90, 0xff0000, v90
	v_lshlrev_b32_e32 v93, 24, v93
	v_lshlrev_b32_e32 v92, 24, v92
	v_pk_add_f32 v[68:69], v[68:69], s[14:15] op_sel_hi:[1,0]
	v_lshlrev_b32_e32 v77, 8, v77
	v_lshlrev_b32_e32 v76, 8, v76
	v_or_b32_e32 v91, v91, v93
	v_or_b32_e32 v90, v90, v92
	v_and_b32_e32 v77, 0xff00, v77
	v_and_b32_e32 v76, 0xff00, v76
	v_or_b32_sdwa v69, v91, v69 dst_sel:DWORD dst_unused:UNUSED_PAD src0_sel:DWORD src1_sel:BYTE_0
	v_or_b32_sdwa v68, v90, v68 dst_sel:DWORD dst_unused:UNUSED_PAD src0_sel:DWORD src1_sel:BYTE_0
	v_or_b32_e32 v69, v69, v77
	v_or_b32_e32 v68, v68, v76
	v_mul_f32_e32 v77, 0x44800000, v16
	ds_write_b128 v89, v[66:69] offset:528
	v_mul_f32_e32 v69, 0x44800000, v12
	v_med3_f32 v90, v77, s60, v86
	v_mul_f32_e32 v77, 0x44800000, v28
	v_med3_f32 v76, v69, s60, v86
	v_mul_f32_e32 v91, 0x44800000, v32
	v_med3_f32 v77, v77, s60, v86
	v_mul_f32_e32 v67, 0x44800000, v8
	v_med3_f32 v91, v91, s60, v86
	v_pk_add_f32 v[76:77], v[76:77], s[14:15] op_sel_hi:[1,0]
	v_mul_f32_e32 v66, 0x44800000, v4
	v_med3_f32 v68, v67, s60, v86
	v_mul_f32_e32 v67, 0x44800000, v20
	v_mul_f32_e32 v69, 0x44800000, v24
	v_pk_add_f32 v[90:91], v[90:91], s[14:15] op_sel_hi:[1,0]
	v_lshlrev_b32_e32 v77, 16, v77
	v_med3_f32 v66, v66, s60, v86
	v_med3_f32 v67, v67, s60, v86
	v_med3_f32 v69, v69, s60, v86
	v_and_b32_e32 v77, 0xff0000, v77
	v_lshlrev_b32_e32 v91, 24, v91
	v_pk_add_f32 v[66:67], v[66:67], s[14:15] op_sel_hi:[1,0]
	v_pk_add_f32 v[68:69], v[68:69], s[14:15] op_sel_hi:[1,0]
	v_lshlrev_b32_e32 v76, 16, v76
	v_or_b32_e32 v77, v77, v91
	v_mul_f32_e32 v91, 0x44800000, v48
	v_lshlrev_b32_e32 v69, 8, v69
	v_and_b32_e32 v76, 0xff0000, v76
	v_lshlrev_b32_e32 v90, 24, v90
	v_or_b32_sdwa v67, v77, v67 dst_sel:DWORD dst_unused:UNUSED_PAD src0_sel:DWORD src1_sel:BYTE_0
	v_mul_f32_e32 v77, 0x44800000, v44
	v_med3_f32 v92, v91, s60, v86
	v_mul_f32_e32 v91, 0x44800000, v60
	v_lshlrev_b32_e32 v68, 8, v68
	v_and_b32_e32 v69, 0xff00, v69
	v_or_b32_e32 v76, v76, v90
	v_med3_f32 v90, v77, s60, v86
	v_mul_f32_e32 v93, 0x44800000, v64
	v_med3_f32 v91, v91, s60, v86
	v_and_b32_e32 v68, 0xff00, v68
	v_or_b32_sdwa v66, v76, v66 dst_sel:DWORD dst_unused:UNUSED_PAD src0_sel:DWORD src1_sel:BYTE_0
	v_or_b32_e32 v67, v67, v69
	v_mul_f32_e32 v69, 0x44800000, v40
	v_mul_f32_e32 v77, 0x44800000, v56
	v_med3_f32 v93, v93, s60, v86
	v_pk_add_f32 v[90:91], v[90:91], s[14:15] op_sel_hi:[1,0]
	v_or_b32_e32 v66, v66, v68
	v_mul_f32_e32 v68, 0x44800000, v36
	v_med3_f32 v76, v69, s60, v86
	v_mul_f32_e32 v69, 0x44800000, v52
	v_med3_f32 v77, v77, s60, v86
	v_pk_add_f32 v[92:93], v[92:93], s[14:15] op_sel_hi:[1,0]
	v_lshlrev_b32_e32 v91, 16, v91
	v_lshlrev_b32_e32 v90, 16, v90
	v_med3_f32 v68, v68, s60, v86
	v_med3_f32 v69, v69, s60, v86
	v_pk_add_f32 v[76:77], v[76:77], s[14:15] op_sel_hi:[1,0]
	v_and_b32_e32 v91, 0xff0000, v91
	v_and_b32_e32 v90, 0xff0000, v90
	v_lshlrev_b32_e32 v93, 24, v93
	v_lshlrev_b32_e32 v92, 24, v92
	v_pk_add_f32 v[68:69], v[68:69], s[14:15] op_sel_hi:[1,0]
	v_lshlrev_b32_e32 v77, 8, v77
	v_lshlrev_b32_e32 v76, 8, v76
	v_or_b32_e32 v91, v91, v93
	v_or_b32_e32 v90, v90, v92
	v_and_b32_e32 v77, 0xff00, v77
	v_and_b32_e32 v76, 0xff00, v76
	v_or_b32_sdwa v69, v91, v69 dst_sel:DWORD dst_unused:UNUSED_PAD src0_sel:DWORD src1_sel:BYTE_0
	v_or_b32_sdwa v68, v90, v68 dst_sel:DWORD dst_unused:UNUSED_PAD src0_sel:DWORD src1_sel:BYTE_0
	v_or_b32_e32 v69, v69, v77
	v_or_b32_e32 v68, v68, v76
	v_mul_f32_e32 v77, 0x44800000, v17
	ds_write_b128 v89, v[66:69] offset:1056
	v_mul_f32_e32 v69, 0x44800000, v13
	v_med3_f32 v90, v77, s60, v86
	v_mul_f32_e32 v77, 0x44800000, v29
	v_med3_f32 v76, v69, s60, v86
	v_mul_f32_e32 v91, 0x44800000, v33
	v_med3_f32 v77, v77, s60, v86
	v_mul_f32_e32 v67, 0x44800000, v9
	v_med3_f32 v91, v91, s60, v86
	v_pk_add_f32 v[76:77], v[76:77], s[14:15] op_sel_hi:[1,0]
	v_mul_f32_e32 v66, 0x44800000, v5
	v_med3_f32 v68, v67, s60, v86
	v_mul_f32_e32 v67, 0x44800000, v21
	v_mul_f32_e32 v69, 0x44800000, v25
	v_pk_add_f32 v[90:91], v[90:91], s[14:15] op_sel_hi:[1,0]
	v_lshlrev_b32_e32 v77, 16, v77
	v_med3_f32 v66, v66, s60, v86
	v_med3_f32 v67, v67, s60, v86
	v_med3_f32 v69, v69, s60, v86
	v_and_b32_e32 v77, 0xff0000, v77
	v_lshlrev_b32_e32 v91, 24, v91
	v_pk_add_f32 v[66:67], v[66:67], s[14:15] op_sel_hi:[1,0]
	v_pk_add_f32 v[68:69], v[68:69], s[14:15] op_sel_hi:[1,0]
	v_lshlrev_b32_e32 v76, 16, v76
	v_or_b32_e32 v77, v77, v91
	v_mul_f32_e32 v91, 0x44800000, v49
	v_lshlrev_b32_e32 v69, 8, v69
	v_and_b32_e32 v76, 0xff0000, v76
	v_lshlrev_b32_e32 v90, 24, v90
	v_or_b32_sdwa v67, v77, v67 dst_sel:DWORD dst_unused:UNUSED_PAD src0_sel:DWORD src1_sel:BYTE_0
	v_mul_f32_e32 v77, 0x44800000, v45
	v_med3_f32 v92, v91, s60, v86
	v_mul_f32_e32 v91, 0x44800000, v61
	v_lshlrev_b32_e32 v68, 8, v68
	v_and_b32_e32 v69, 0xff00, v69
	v_or_b32_e32 v76, v76, v90
	v_med3_f32 v90, v77, s60, v86
	v_mul_f32_e32 v93, 0x44800000, v65
	v_med3_f32 v91, v91, s60, v86
	v_and_b32_e32 v68, 0xff00, v68
	v_or_b32_sdwa v66, v76, v66 dst_sel:DWORD dst_unused:UNUSED_PAD src0_sel:DWORD src1_sel:BYTE_0
	v_or_b32_e32 v67, v67, v69
	v_mul_f32_e32 v69, 0x44800000, v41
	v_mul_f32_e32 v77, 0x44800000, v57
	v_med3_f32 v93, v93, s60, v86
	v_pk_add_f32 v[90:91], v[90:91], s[14:15] op_sel_hi:[1,0]
	v_or_b32_e32 v66, v66, v68
	v_mul_f32_e32 v68, 0x44800000, v37
	v_med3_f32 v76, v69, s60, v86
	v_mul_f32_e32 v69, 0x44800000, v53
	v_med3_f32 v77, v77, s60, v86
	v_pk_add_f32 v[92:93], v[92:93], s[14:15] op_sel_hi:[1,0]
	v_lshlrev_b32_e32 v91, 16, v91
	v_lshlrev_b32_e32 v90, 16, v90
	v_med3_f32 v68, v68, s60, v86
	v_med3_f32 v69, v69, s60, v86
	v_pk_add_f32 v[76:77], v[76:77], s[14:15] op_sel_hi:[1,0]
	v_and_b32_e32 v91, 0xff0000, v91
	v_and_b32_e32 v90, 0xff0000, v90
	v_lshlrev_b32_e32 v93, 24, v93
	v_lshlrev_b32_e32 v92, 24, v92
	v_pk_add_f32 v[68:69], v[68:69], s[14:15] op_sel_hi:[1,0]
	v_lshlrev_b32_e32 v77, 8, v77
	v_lshlrev_b32_e32 v76, 8, v76
	v_or_b32_e32 v91, v91, v93
	v_or_b32_e32 v90, v90, v92
	v_and_b32_e32 v77, 0xff00, v77
	v_and_b32_e32 v76, 0xff00, v76
	v_or_b32_sdwa v69, v91, v69 dst_sel:DWORD dst_unused:UNUSED_PAD src0_sel:DWORD src1_sel:BYTE_0
	v_or_b32_sdwa v68, v90, v68 dst_sel:DWORD dst_unused:UNUSED_PAD src0_sel:DWORD src1_sel:BYTE_0
	v_or_b32_e32 v69, v69, v77
	v_or_b32_e32 v68, v68, v76
	ds_write_b128 v89, v[66:69] offset:1584
	s_mov_b64 s[20:21], 0

.LBB0_3196:
	s_cmp_eq_u32 s59, 0
	s_cbranch_scc1 .LBB0_3200
	s_mov_b64 s[22:23], exec
	v_mbcnt_lo_u32_b32 v66, s22, 0
	v_mbcnt_hi_u32_b32 v66, s23, v66
	v_cmp_eq_u32_e32 vcc, 0, v66
	s_and_saveexec_b64 s[20:21], vcc
	s_cbranch_execz .LBB0_3199
	s_bcnt1_i32_b64 s6, s[22:23]
	v_mov_b32_e32 v67, s6
	v_mov_b32_e32 v67, v253

.Lec_7_rest:
	s_or_b64 exec, exec, s[2:3]
	s_mov_b32 s15, s65
	s_mov_b32 s61, s20
	s_mov_b32 s14, s66
	s_mov_b32 s25, s63
	s_mov_b32 s60, s64
	s_mov_b32 s24, s62
	s_mov_b64 s[16:17], s[18:19]
	s_mov_b64 s[20:21], -1
	s_mov_b64 s[2:3], 0
	s_cmp_lt_i32 s65, 2
	s_mov_b64 s[18:19], 0
	s_cbranch_scc1 .LBB0_3434
	s_cmp_eq_u32 s15, 2
	s_mov_b64 s[18:19], -1
	s_cbranch_scc0 .LBB0_3430
	s_waitcnt vmcnt(12)
	v_mul_f32_e32 v77, 0x44800000, v14
	v_mul_f32_e32 v69, 0x44800000, v10
	v_med3_f32 v90, v77, s55, v86
	s_waitcnt vmcnt(9)
	v_mul_f32_e32 v77, 0x44800000, v26
	v_med3_f32 v76, v69, s55, v86
	s_waitcnt vmcnt(8)
	v_mul_f32_e32 v89, 0x44800000, v30
	v_med3_f32 v77, v77, s55, v86
	v_mul_f32_e32 v67, 0x44800000, v6
	v_med3_f32 v91, v89, s55, v86
	v_pk_add_f32 v[76:77], v[76:77], s[12:13] op_sel_hi:[1,0]
	v_mul_f32_e32 v66, 0x44800000, v2
	v_med3_f32 v68, v67, s55, v86
	v_mul_f32_e32 v67, 0x44800000, v18
	v_mul_f32_e32 v69, 0x44800000, v22
	v_pk_add_f32 v[90:91], v[90:91], s[12:13] op_sel_hi:[1,0]
	v_lshlrev_b32_e32 v77, 16, v77
	v_med3_f32 v66, v66, s55, v86
	v_med3_f32 v67, v67, s55, v86
	v_med3_f32 v69, v69, s55, v86
	v_and_b32_e32 v77, 0xff0000, v77
	v_lshlrev_b32_e32 v89, 24, v91
	v_pk_add_f32 v[66:67], v[66:67], s[12:13] op_sel_hi:[1,0]
	v_pk_add_f32 v[68:69], v[68:69], s[12:13] op_sel_hi:[1,0]
	v_lshlrev_b32_e32 v76, 16, v76
	v_or_b32_e32 v77, v77, v89
	s_waitcnt vmcnt(4)
	v_mul_f32_e32 v89, 0x44800000, v46
	v_lshlrev_b32_e32 v69, 8, v69
	v_and_b32_e32 v76, 0xff0000, v76
	v_lshlrev_b32_e32 v90, 24, v90
	v_or_b32_sdwa v67, v77, v67 dst_sel:DWORD dst_unused:UNUSED_PAD src0_sel:DWORD src1_sel:BYTE_0
	v_mul_f32_e32 v77, 0x44800000, v42
	v_med3_f32 v92, v89, s55, v86
	s_waitcnt vmcnt(1)
	v_mul_f32_e32 v89, 0x44800000, v58
	v_lshlrev_b32_e32 v68, 8, v68
	v_and_b32_e32 v69, 0xff00, v69
	v_or_b32_e32 v76, v76, v90
	v_med3_f32 v90, v77, s55, v86
	s_waitcnt vmcnt(0)
	v_mul_f32_e32 v93, 0x44800000, v62
	v_med3_f32 v91, v89, s55, v86
	v_and_b32_e32 v68, 0xff00, v68
	v_or_b32_sdwa v66, v76, v66 dst_sel:DWORD dst_unused:UNUSED_PAD src0_sel:DWORD src1_sel:BYTE_0
	v_or_b32_e32 v67, v67, v69
	v_mul_f32_e32 v69, 0x44800000, v38
	v_mul_f32_e32 v77, 0x44800000, v54
	v_med3_f32 v93, v93, s55, v86
	v_pk_add_f32 v[90:91], v[90:91], s[12:13] op_sel_hi:[1,0]
	v_or_b32_e32 v66, v66, v68
	v_mul_f32_e32 v68, 0x44800000, v34
	v_med3_f32 v76, v69, s55, v86
	v_mul_f32_e32 v69, 0x44800000, v50
	v_med3_f32 v77, v77, s55, v86
	v_pk_add_f32 v[92:93], v[92:93], s[12:13] op_sel_hi:[1,0]
	v_lshlrev_b32_e32 v89, 16, v91
	v_lshlrev_b32_e32 v90, 16, v90
	v_med3_f32 v68, v68, s55, v86
	v_med3_f32 v69, v69, s55, v86
	v_pk_add_f32 v[76:77], v[76:77], s[12:13] op_sel_hi:[1,0]
	v_and_b32_e32 v89, 0xff0000, v89
	v_and_b32_e32 v90, 0xff0000, v90
	v_lshlrev_b32_e32 v91, 24, v93
	v_lshlrev_b32_e32 v92, 24, v92
	v_pk_add_f32 v[68:69], v[68:69], s[12:13] op_sel_hi:[1,0]
	v_lshlrev_b32_e32 v77, 8, v77
	v_lshlrev_b32_e32 v76, 8, v76
	v_or_b32_e32 v89, v89, v91
	v_or_b32_e32 v90, v90, v92
	v_and_b32_e32 v77, 0xff00, v77
	v_and_b32_e32 v76, 0xff00, v76
	v_or_b32_sdwa v69, v89, v69 dst_sel:DWORD dst_unused:UNUSED_PAD src0_sel:DWORD src1_sel:BYTE_0
	v_or_b32_sdwa v68, v90, v68 dst_sel:DWORD dst_unused:UNUSED_PAD src0_sel:DWORD src1_sel:BYTE_0
	v_or_b32_e32 v69, v69, v77
	v_or_b32_e32 v68, v68, v76
	v_add_u32_e32 v89, v78, v75
	v_mul_f32_e32 v77, 0x44800000, v15
	ds_write_b128 v89, v[66:69]
	v_mul_f32_e32 v69, 0x44800000, v11
	v_med3_f32 v90, v77, s55, v86
	v_mul_f32_e32 v77, 0x44800000, v27
	v_med3_f32 v76, v69, s55, v86
	v_mul_f32_e32 v91, 0x44800000, v31
	v_med3_f32 v77, v77, s55, v86
	v_mul_f32_e32 v67, 0x44800000, v7
	v_med3_f32 v91, v91, s55, v86
	v_pk_add_f32 v[76:77], v[76:77], s[12:13] op_sel_hi:[1,0]
	v_mul_f32_e32 v66, 0x44800000, v3
	v_med3_f32 v68, v67, s55, v86
	v_mul_f32_e32 v67, 0x44800000, v19
	v_mul_f32_e32 v69, 0x44800000, v23
	v_pk_add_f32 v[90:91], v[90:91], s[12:13] op_sel_hi:[1,0]
	v_lshlrev_b32_e32 v77, 16, v77
	v_med3_f32 v66, v66, s55, v86
	v_med3_f32 v67, v67, s55, v86
	v_med3_f32 v69, v69, s55, v86
	v_and_b32_e32 v77, 0xff0000, v77
	v_lshlrev_b32_e32 v91, 24, v91
	v_pk_add_f32 v[66:67], v[66:67], s[12:13] op_sel_hi:[1,0]
	v_pk_add_f32 v[68:69], v[68:69], s[12:13] op_sel_hi:[1,0]
	v_lshlrev_b32_e32 v76, 16, v76
	v_or_b32_e32 v77, v77, v91
	v_mul_f32_e32 v91, 0x44800000, v47
	v_lshlrev_b32_e32 v69, 8, v69
	v_and_b32_e32 v76, 0xff0000, v76
	v_lshlrev_b32_e32 v90, 24, v90
	v_or_b32_sdwa v67, v77, v67 dst_sel:DWORD dst_unused:UNUSED_PAD src0_sel:DWORD src1_sel:BYTE_0
	v_mul_f32_e32 v77, 0x44800000, v43
	v_med3_f32 v92, v91, s55, v86
	v_mul_f32_e32 v91, 0x44800000, v59
	v_lshlrev_b32_e32 v68, 8, v68
	v_and_b32_e32 v69, 0xff00, v69
	v_or_b32_e32 v76, v76, v90
	v_med3_f32 v90, v77, s55, v86
	v_mul_f32_e32 v93, 0x44800000, v63
	v_med3_f32 v91, v91, s55, v86
	v_and_b32_e32 v68, 0xff00, v68
	v_or_b32_sdwa v66, v76, v66 dst_sel:DWORD dst_unused:UNUSED_PAD src0_sel:DWORD src1_sel:BYTE_0
	v_or_b32_e32 v67, v67, v69
	v_mul_f32_e32 v69, 0x44800000, v39
	v_mul_f32_e32 v77, 0x44800000, v55
	v_med3_f32 v93, v93, s55, v86
	v_pk_add_f32 v[90:91], v[90:91], s[12:13] op_sel_hi:[1,0]
	v_or_b32_e32 v66, v66, v68
	v_mul_f32_e32 v68, 0x44800000, v35
	v_med3_f32 v76, v69, s55, v86
	v_mul_f32_e32 v69, 0x44800000, v51
	v_med3_f32 v77, v77, s55, v86
	v_pk_add_f32 v[92:93], v[92:93], s[12:13] op_sel_hi:[1,0]
	v_lshlrev_b32_e32 v91, 16, v91
	v_lshlrev_b32_e32 v90, 16, v90
	v_med3_f32 v68, v68, s55, v86
	v_med3_f32 v69, v69, s55, v86
	v_pk_add_f32 v[76:77], v[76:77], s[12:13] op_sel_hi:[1,0]
	v_and_b32_e32 v91, 0xff0000, v91
	v_and_b32_e32 v90, 0xff0000, v90
	v_lshlrev_b32_e32 v93, 24, v93
	v_lshlrev_b32_e32 v92, 24, v92
	v_pk_add_f32 v[68:69], v[68:69], s[12:13] op_sel_hi:[1,0]
	v_lshlrev_b32_e32 v77, 8, v77
	v_lshlrev_b32_e32 v76, 8, v76
	v_or_b32_e32 v91, v91, v93
	v_or_b32_e32 v90, v90, v92
	v_and_b32_e32 v77, 0xff00, v77
	v_and_b32_e32 v76, 0xff00, v76
	v_or_b32_sdwa v69, v91, v69 dst_sel:DWORD dst_unused:UNUSED_PAD src0_sel:DWORD src1_sel:BYTE_0
	v_or_b32_sdwa v68, v90, v68 dst_sel:DWORD dst_unused:UNUSED_PAD src0_sel:DWORD src1_sel:BYTE_0
	v_or_b32_e32 v69, v69, v77
	v_or_b32_e32 v68, v68, v76
	v_mul_f32_e32 v77, 0x44800000, v16
	ds_write_b128 v89, v[66:69] offset:528
	v_mul_f32_e32 v69, 0x44800000, v12
	v_med3_f32 v90, v77, s55, v86
	v_mul_f32_e32 v77, 0x44800000, v28
	v_med3_f32 v76, v69, s55, v86
	v_mul_f32_e32 v91, 0x44800000, v32
	v_med3_f32 v77, v77, s55, v86
	v_mul_f32_e32 v67, 0x44800000, v8
	v_med3_f32 v91, v91, s55, v86
	v_pk_add_f32 v[76:77], v[76:77], s[12:13] op_sel_hi:[1,0]
	v_mul_f32_e32 v66, 0x44800000, v4
	v_med3_f32 v68, v67, s55, v86
	v_mul_f32_e32 v67, 0x44800000, v20
	v_mul_f32_e32 v69, 0x44800000, v24
	v_pk_add_f32 v[90:91], v[90:91], s[12:13] op_sel_hi:[1,0]
	v_lshlrev_b32_e32 v77, 16, v77
	v_med3_f32 v66, v66, s55, v86
	v_med3_f32 v67, v67, s55, v86
	v_med3_f32 v69, v69, s55, v86
	v_and_b32_e32 v77, 0xff0000, v77
	v_lshlrev_b32_e32 v91, 24, v91
	v_pk_add_f32 v[66:67], v[66:67], s[12:13] op_sel_hi:[1,0]
	v_pk_add_f32 v[68:69], v[68:69], s[12:13] op_sel_hi:[1,0]
	v_lshlrev_b32_e32 v76, 16, v76
	v_or_b32_e32 v77, v77, v91
	v_mul_f32_e32 v91, 0x44800000, v48
	v_lshlrev_b32_e32 v69, 8, v69
	v_and_b32_e32 v76, 0xff0000, v76
	v_lshlrev_b32_e32 v90, 24, v90
	v_or_b32_sdwa v67, v77, v67 dst_sel:DWORD dst_unused:UNUSED_PAD src0_sel:DWORD src1_sel:BYTE_0
	v_mul_f32_e32 v77, 0x44800000, v44
	v_med3_f32 v92, v91, s55, v86
	v_mul_f32_e32 v91, 0x44800000, v60
	v_lshlrev_b32_e32 v68, 8, v68
	v_and_b32_e32 v69, 0xff00, v69
	v_or_b32_e32 v76, v76, v90
	v_med3_f32 v90, v77, s55, v86
	v_mul_f32_e32 v93, 0x44800000, v64
	v_med3_f32 v91, v91, s55, v86
	v_and_b32_e32 v68, 0xff00, v68
	v_or_b32_sdwa v66, v76, v66 dst_sel:DWORD dst_unused:UNUSED_PAD src0_sel:DWORD src1_sel:BYTE_0
	v_or_b32_e32 v67, v67, v69
	v_mul_f32_e32 v69, 0x44800000, v40
	v_mul_f32_e32 v77, 0x44800000, v56
	v_med3_f32 v93, v93, s55, v86
	v_pk_add_f32 v[90:91], v[90:91], s[12:13] op_sel_hi:[1,0]
	v_or_b32_e32 v66, v66, v68
	v_mul_f32_e32 v68, 0x44800000, v36
	v_med3_f32 v76, v69, s55, v86
	v_mul_f32_e32 v69, 0x44800000, v52
	v_med3_f32 v77, v77, s55, v86
	v_pk_add_f32 v[92:93], v[92:93], s[12:13] op_sel_hi:[1,0]
	v_lshlrev_b32_e32 v91, 16, v91
	v_lshlrev_b32_e32 v90, 16, v90
	v_med3_f32 v68, v68, s55, v86
	v_med3_f32 v69, v69, s55, v86
	v_pk_add_f32 v[76:77], v[76:77], s[12:13] op_sel_hi:[1,0]
	v_and_b32_e32 v91, 0xff0000, v91
	v_and_b32_e32 v90, 0xff0000, v90
	v_lshlrev_b32_e32 v93, 24, v93
	v_lshlrev_b32_e32 v92, 24, v92
	v_pk_add_f32 v[68:69], v[68:69], s[12:13] op_sel_hi:[1,0]
	v_lshlrev_b32_e32 v77, 8, v77
	v_lshlrev_b32_e32 v76, 8, v76
	v_or_b32_e32 v91, v91, v93
	v_or_b32_e32 v90, v90, v92
	v_and_b32_e32 v77, 0xff00, v77
	v_and_b32_e32 v76, 0xff00, v76
	v_or_b32_sdwa v69, v91, v69 dst_sel:DWORD dst_unused:UNUSED_PAD src0_sel:DWORD src1_sel:BYTE_0
	v_or_b32_sdwa v68, v90, v68 dst_sel:DWORD dst_unused:UNUSED_PAD src0_sel:DWORD src1_sel:BYTE_0
	v_or_b32_e32 v69, v69, v77
	v_or_b32_e32 v68, v68, v76
	v_mul_f32_e32 v77, 0x44800000, v17
	ds_write_b128 v89, v[66:69] offset:1056
	v_mul_f32_e32 v69, 0x44800000, v13
	v_med3_f32 v90, v77, s55, v86
	v_mul_f32_e32 v77, 0x44800000, v29
	v_med3_f32 v76, v69, s55, v86
	v_mul_f32_e32 v91, 0x44800000, v33
	v_med3_f32 v77, v77, s55, v86
	v_mul_f32_e32 v67, 0x44800000, v9
	v_med3_f32 v91, v91, s55, v86
	v_pk_add_f32 v[76:77], v[76:77], s[12:13] op_sel_hi:[1,0]
	v_mul_f32_e32 v66, 0x44800000, v5
	v_med3_f32 v68, v67, s55, v86
	v_mul_f32_e32 v67, 0x44800000, v21
	v_mul_f32_e32 v69, 0x44800000, v25
	v_pk_add_f32 v[90:91], v[90:91], s[12:13] op_sel_hi:[1,0]
	v_lshlrev_b32_e32 v77, 16, v77
	v_med3_f32 v66, v66, s55, v86
	v_med3_f32 v67, v67, s55, v86
	v_med3_f32 v69, v69, s55, v86
	v_and_b32_e32 v77, 0xff0000, v77
	v_lshlrev_b32_e32 v91, 24, v91
	v_pk_add_f32 v[66:67], v[66:67], s[12:13] op_sel_hi:[1,0]
	v_pk_add_f32 v[68:69], v[68:69], s[12:13] op_sel_hi:[1,0]
	v_lshlrev_b32_e32 v76, 16, v76
	v_or_b32_e32 v77, v77, v91
	v_mul_f32_e32 v91, 0x44800000, v49
	v_lshlrev_b32_e32 v69, 8, v69
	v_and_b32_e32 v76, 0xff0000, v76
	v_lshlrev_b32_e32 v90, 24, v90
	v_or_b32_sdwa v67, v77, v67 dst_sel:DWORD dst_unused:UNUSED_PAD src0_sel:DWORD src1_sel:BYTE_0
	v_mul_f32_e32 v77, 0x44800000, v45
	v_med3_f32 v92, v91, s55, v86
	v_mul_f32_e32 v91, 0x44800000, v61
	v_lshlrev_b32_e32 v68, 8, v68
	v_and_b32_e32 v69, 0xff00, v69
	v_or_b32_e32 v76, v76, v90
	v_med3_f32 v90, v77, s55, v86
	v_mul_f32_e32 v93, 0x44800000, v65
	v_med3_f32 v91, v91, s55, v86
	v_and_b32_e32 v68, 0xff00, v68
	v_or_b32_sdwa v66, v76, v66 dst_sel:DWORD dst_unused:UNUSED_PAD src0_sel:DWORD src1_sel:BYTE_0
	v_or_b32_e32 v67, v67, v69
	v_mul_f32_e32 v69, 0x44800000, v41
	v_mul_f32_e32 v77, 0x44800000, v57
	v_med3_f32 v93, v93, s55, v86
	v_pk_add_f32 v[90:91], v[90:91], s[12:13] op_sel_hi:[1,0]
	v_or_b32_e32 v66, v66, v68
	v_mul_f32_e32 v68, 0x44800000, v37
	v_med3_f32 v76, v69, s55, v86
	v_mul_f32_e32 v69, 0x44800000, v53
	v_med3_f32 v77, v77, s55, v86
	v_pk_add_f32 v[92:93], v[92:93], s[12:13] op_sel_hi:[1,0]
	v_lshlrev_b32_e32 v91, 16, v91
	v_lshlrev_b32_e32 v90, 16, v90
	v_med3_f32 v68, v68, s55, v86
	v_med3_f32 v69, v69, s55, v86
	v_pk_add_f32 v[76:77], v[76:77], s[12:13] op_sel_hi:[1,0]
	v_and_b32_e32 v91, 0xff0000, v91
	v_and_b32_e32 v90, 0xff0000, v90
	v_lshlrev_b32_e32 v93, 24, v93
	v_lshlrev_b32_e32 v92, 24, v92
	v_pk_add_f32 v[68:69], v[68:69], s[12:13] op_sel_hi:[1,0]
	v_lshlrev_b32_e32 v77, 8, v77
	v_lshlrev_b32_e32 v76, 8, v76
	v_or_b32_e32 v91, v91, v93
	v_or_b32_e32 v90, v90, v92
	v_and_b32_e32 v77, 0xff00, v77
	v_and_b32_e32 v76, 0xff00, v76
	v_or_b32_sdwa v69, v91, v69 dst_sel:DWORD dst_unused:UNUSED_PAD src0_sel:DWORD src1_sel:BYTE_0
	v_or_b32_sdwa v68, v90, v68 dst_sel:DWORD dst_unused:UNUSED_PAD src0_sel:DWORD src1_sel:BYTE_0
	v_or_b32_e32 v69, v69, v77
	v_or_b32_e32 v68, v68, v76
	ds_write_b128 v89, v[66:69] offset:1584
	s_mov_b64 s[18:19], 0

.LBB0_3438:
	s_cmp_eq_u32 s54, 0
	s_cbranch_scc1 .LBB0_3442
	s_mov_b64 s[20:21], exec
	v_mbcnt_lo_u32_b32 v66, s20, 0
	v_mbcnt_hi_u32_b32 v66, s21, v66
	v_cmp_eq_u32_e32 vcc, 0, v66
	s_and_saveexec_b64 s[18:19], vcc
	s_cbranch_execz .LBB0_3441
	s_bcnt1_i32_b64 s4, s[20:21]
	v_mov_b32_e32 v67, s4
	v_mov_b32_e32 v67, v253
